# int8 GEMM phases (QKV, dense gate/up, mixer in-projection): row / column scale loads issued at the start of each unit instead of the top of the epilogue, epilogue drain removed; 115 converter workgrou
# baseline (speedup 1.0000x reference)
.LBB0_527:
	v_add_u32_e32 v130, 0, v202
	v_add_u32_e32 v131, 0x10000, v130
	v_add_u32_e32 v130, 0x14000, v130
	ds_read_b128 v[158:161], v131
	ds_read_b128 v[154:157], v131 offset:1024
	ds_read_b128 v[150:153], v131 offset:2048
	ds_read_b128 v[142:145], v131 offset:3072
	ds_read_b128 v[146:149], v130
	ds_read_b128 v[138:141], v130 offset:1024
	ds_read_b128 v[134:137], v130 offset:2048
	ds_read_b128 v[130:133], v130 offset:3072
	s_add_u32 s51, s44, s66
	s_addc_u32 s62, s45, s67
	s_add_u32 s8, s51, 0x80
	s_addc_u32 s9, s62, 0
	v_mov_b32_e32 v205, v196
	ds_read_b128 v[190:193], v204
	ds_read_b128 v[186:189], v204 offset:1024
	ds_read_b128 v[182:185], v204 offset:2048
	ds_read_b128 v[178:181], v204 offset:3072
	ds_read_b128 v[174:177], v204 offset:4096
	ds_read_b128 v[170:173], v204 offset:5120
	ds_read_b128 v[166:169], v204 offset:6144
	ds_read_b128 v[162:165], v204 offset:7168
	s_add_i32 m0, s1, 0x8000
	s_nop 0
	global_load_lds_dwordx4 v205, s[8:9]
	v_mov_b32_e32 v205, v198
	s_add_i32 m0, s1, 0xa000
	s_nop 0
	global_load_lds_dwordx4 v205, s[8:9]
	s_add_u32 s8, s51, 0x40080
	s_addc_u32 s9, s62, 0
	v_mov_b32_e32 v205, v196
	s_add_i32 m0, s1, 0xc000
	s_nop 0
	global_load_lds_dwordx4 v205, s[8:9]
	v_mov_b32_e32 v205, v198
	s_add_i32 m0, s1, 0xe000
	s_cmp_lg_u32 s49, -2
	global_load_lds_dwordx4 v205, s[8:9]
	v_lshl_or_b32 v242, s61, 8, v203
	v_lshl_add_u32 v240, s33, 8, v201
	v_ashrrev_i32_e32 v243, 31, v242
	v_ashrrev_i32_e32 v241, 31, v240
	v_lshl_add_u64 v[242:243], v[242:243], 2, s[6:7]
	v_lshl_add_u64 v[240:241], v[240:241], 2, s[38:39]
	global_load_dwordx4 v[210:213], v[242:243], off
	global_load_dwordx4 v[214:217], v[242:243], off offset:16
	global_load_dwordx4 v[218:221], v[242:243], off offset:512
	global_load_dwordx4 v[222:225], v[242:243], off offset:528
	global_load_dword v232, v[240:241], off
	global_load_dword v233, v[240:241], off offset:64
	global_load_dword v234, v[240:241], off offset:128
	global_load_dword v235, v[240:241], off offset:192
	global_load_dword v236, v[240:241], off offset:512
	global_load_dword v237, v[240:241], off offset:576
	global_load_dword v238, v[240:241], off offset:640
	global_load_dword v239, v[240:241], off offset:704
	s_cselect_b64 s[80:81], -1, 0
	s_and_b64 vcc, exec, s[80:81]
	s_cbranch_vccnz .LBB0_530
	s_mov_b64 s[42:43], 0
	s_andn2_b64 vcc, exec, s[2:3]
	s_mov_b64 s[8:9], s[46:47]
	s_mov_b64 s[40:41], s[44:45]
	s_cbranch_vccnz .LBB0_531
	s_mov_b64 s[42:43], -1
	s_mov_b64 s[8:9], s[64:65]
	s_mov_b64 s[40:41], s[52:53]
	s_mov_b32 s0, s50
	s_mov_b32 s30, s48
	s_branch .LBB0_531

.LBB0_531:
	s_waitcnt vmcnt(20)
	s_waitcnt lgkmcnt(0)
	s_barrier
	s_setprio 1
	v_mfma_i32_16x16x64_i8 v[18:21], v[158:161], v[190:193], 0
	s_nop 0
	v_mfma_i32_16x16x64_i8 v[18:21], v[154:157], v[186:189], v[18:21]
	v_mfma_i32_16x16x64_i8 v[22:25], v[150:153], v[190:193], 0
	s_nop 0
	v_mfma_i32_16x16x64_i8 v[22:25], v[142:145], v[186:189], v[22:25]
	v_mfma_i32_16x16x64_i8 v[26:29], v[146:149], v[190:193], 0
	s_nop 0
	v_mfma_i32_16x16x64_i8 v[26:29], v[138:141], v[186:189], v[26:29]
	v_mfma_i32_16x16x64_i8 v[34:37], v[134:137], v[190:193], 0
	s_nop 0
	v_mfma_i32_16x16x64_i8 v[34:37], v[130:133], v[186:189], v[34:37]
	v_mfma_i32_16x16x64_i8 v[50:53], v[158:161], v[182:185], 0
	s_nop 0
	v_mfma_i32_16x16x64_i8 v[50:53], v[154:157], v[178:181], v[50:53]
	v_mfma_i32_16x16x64_i8 v[62:65], v[150:153], v[182:185], 0
	s_nop 0
	v_mfma_i32_16x16x64_i8 v[62:65], v[142:145], v[178:181], v[62:65]
	v_mfma_i32_16x16x64_i8 v[54:57], v[146:149], v[182:185], 0
	s_nop 0
	v_mfma_i32_16x16x64_i8 v[54:57], v[138:141], v[178:181], v[54:57]
	v_mfma_i32_16x16x64_i8 v[66:69], v[134:137], v[182:185], 0
	s_nop 0
	v_mfma_i32_16x16x64_i8 v[66:69], v[130:133], v[178:181], v[66:69]
	v_mfma_i32_16x16x64_i8 v[82:85], v[158:161], v[174:177], 0
	s_nop 0
	v_mfma_i32_16x16x64_i8 v[82:85], v[154:157], v[170:173], v[82:85]
	v_mfma_i32_16x16x64_i8 v[94:97], v[150:153], v[174:177], 0
	s_nop 0
	v_mfma_i32_16x16x64_i8 v[94:97], v[142:145], v[170:173], v[94:97]
	v_mfma_i32_16x16x64_i8 v[86:89], v[146:149], v[174:177], 0
	s_nop 0
	v_mfma_i32_16x16x64_i8 v[86:89], v[138:141], v[170:173], v[86:89]
	v_mfma_i32_16x16x64_i8 v[98:101], v[134:137], v[174:177], 0
	s_nop 0
	v_mfma_i32_16x16x64_i8 v[98:101], v[130:133], v[170:173], v[98:101]
	v_mfma_i32_16x16x64_i8 v[114:117], v[158:161], v[166:169], 0
	s_nop 0
	v_mfma_i32_16x16x64_i8 v[114:117], v[154:157], v[162:165], v[114:117]
	v_mfma_i32_16x16x64_i8 v[122:125], v[150:153], v[166:169], 0
	s_nop 0
	v_mfma_i32_16x16x64_i8 v[122:125], v[142:145], v[162:165], v[122:125]
	v_mfma_i32_16x16x64_i8 v[118:121], v[146:149], v[166:169], 0
	s_nop 0
	v_mfma_i32_16x16x64_i8 v[118:121], v[138:141], v[162:165], v[118:121]
	v_mfma_i32_16x16x64_i8 v[126:129], v[134:137], v[166:169], 0
	s_nop 0
	v_mfma_i32_16x16x64_i8 v[126:129], v[130:133], v[162:165], v[126:129]
	s_setprio 0
	s_barrier
	s_add_u32 s63, s35, s66
	s_addc_u32 s69, s60, s67
	s_cmp_eq_u32 s49, 12
	s_cselect_b64 s[82:83], -1, 0
	s_and_b64 s[70:71], s[82:83], exec
	s_cselect_b32 s79, s79, s69
	s_cselect_b32 s78, s78, s63
	s_mov_b64 s[70:71], s[78:79]
	v_mov_b32_e32 v205, v197
	s_mov_b32 m0, s19
	s_waitcnt lgkmcnt(0)
	ds_read_b128 v[190:193], v204 offset:16384
	ds_read_b128 v[186:189], v204 offset:17408
	ds_read_b128 v[182:185], v204 offset:18432
	ds_read_b128 v[178:181], v204 offset:19456
	ds_read_b128 v[174:177], v204 offset:20480
	ds_read_b128 v[170:173], v204 offset:21504
	ds_read_b128 v[166:169], v204 offset:22528
	ds_read_b128 v[162:165], v204 offset:23552
	s_nop 0
	global_load_lds_dwordx4 v205, s[70:71]
	v_mov_b32_e32 v205, v199
	s_mov_b32 m0, s20
	s_nop 0
	global_load_lds_dwordx4 v205, s[70:71]
	s_add_u32 s70, s78, 0x40000
	s_addc_u32 s71, s79, 0
	v_mov_b32_e32 v205, v197
	s_mov_b32 m0, s21
	s_nop 0
	global_load_lds_dwordx4 v205, s[70:71]
	v_mov_b32_e32 v205, v199
	s_mov_b32 m0, s22
	s_nop 0
	global_load_lds_dwordx4 v205, s[70:71]
	s_waitcnt vmcnt(18)
	s_waitcnt lgkmcnt(0)
	s_barrier
	s_setprio 1
	v_mfma_i32_16x16x64_i8 v[2:5], v[158:161], v[190:193], 0
	s_nop 0
	v_mfma_i32_16x16x64_i8 v[2:5], v[154:157], v[186:189], v[2:5]
	v_mfma_i32_16x16x64_i8 v[6:9], v[150:153], v[190:193], 0
	s_nop 0
	v_mfma_i32_16x16x64_i8 v[6:9], v[142:145], v[186:189], v[6:9]
	v_mfma_i32_16x16x64_i8 v[10:13], v[146:149], v[190:193], 0
	s_nop 0
	v_mfma_i32_16x16x64_i8 v[10:13], v[138:141], v[186:189], v[10:13]
	v_mfma_i32_16x16x64_i8 v[14:17], v[134:137], v[190:193], 0
	s_nop 0
	v_mfma_i32_16x16x64_i8 v[14:17], v[130:133], v[186:189], v[14:17]
	v_mfma_i32_16x16x64_i8 v[30:33], v[158:161], v[182:185], 0
	s_nop 0
	v_mfma_i32_16x16x64_i8 v[30:33], v[154:157], v[178:181], v[30:33]
	v_mfma_i32_16x16x64_i8 v[42:45], v[150:153], v[182:185], 0
	s_nop 0
	v_mfma_i32_16x16x64_i8 v[42:45], v[142:145], v[178:181], v[42:45]
	v_mfma_i32_16x16x64_i8 v[38:41], v[146:149], v[182:185], 0
	s_nop 0
	v_mfma_i32_16x16x64_i8 v[38:41], v[138:141], v[178:181], v[38:41]
	v_mfma_i32_16x16x64_i8 v[46:49], v[134:137], v[182:185], 0
	s_nop 0
	v_mfma_i32_16x16x64_i8 v[46:49], v[130:133], v[178:181], v[46:49]
	v_mfma_i32_16x16x64_i8 v[58:61], v[158:161], v[174:177], 0
	s_nop 0
	v_mfma_i32_16x16x64_i8 v[58:61], v[154:157], v[170:173], v[58:61]
	v_mfma_i32_16x16x64_i8 v[74:77], v[150:153], v[174:177], 0
	s_nop 0
	v_mfma_i32_16x16x64_i8 v[74:77], v[142:145], v[170:173], v[74:77]
	v_mfma_i32_16x16x64_i8 v[70:73], v[146:149], v[174:177], 0
	s_nop 0
	v_mfma_i32_16x16x64_i8 v[70:73], v[138:141], v[170:173], v[70:73]
	v_mfma_i32_16x16x64_i8 v[78:81], v[134:137], v[174:177], 0
	s_nop 0
	v_mfma_i32_16x16x64_i8 v[78:81], v[130:133], v[170:173], v[78:81]
	v_mfma_i32_16x16x64_i8 v[90:93], v[158:161], v[166:169], 0
	s_nop 0
	v_mfma_i32_16x16x64_i8 v[90:93], v[154:157], v[162:165], v[90:93]
	v_mfma_i32_16x16x64_i8 v[106:109], v[150:153], v[166:169], 0
	s_nop 0
	v_mfma_i32_16x16x64_i8 v[106:109], v[142:145], v[162:165], v[106:109]
	v_mfma_i32_16x16x64_i8 v[102:105], v[146:149], v[166:169], 0
	s_nop 0
	v_mfma_i32_16x16x64_i8 v[102:105], v[138:141], v[162:165], v[102:105]
	v_mfma_i32_16x16x64_i8 v[110:113], v[134:137], v[166:169], 0
	s_nop 0
	v_mfma_i32_16x16x64_i8 v[110:113], v[130:133], v[162:165], v[110:113]
	s_setprio 0
	s_barrier
	s_add_u32 s51, s51, 0x100
	s_addc_u32 s69, s62, 0
	s_and_b64 s[62:63], s[82:83], exec
	s_cselect_b32 s63, s77, s69
	s_cselect_b32 s62, s76, s51
	s_add_u32 s76, s78, 0x80
	s_addc_u32 s77, s79, 0
	s_add_i32 s51, 0, 0x18000
	s_add_i32 s69, 0, 0x1c000
	v_add_u32_e32 v130, s51, v202
	v_add_u32_e32 v131, s69, v202
	ds_read_b128 v[158:161], v130
	ds_read_b128 v[154:157], v130 offset:1024
	ds_read_b128 v[150:153], v130 offset:2048
	ds_read_b128 v[146:149], v130 offset:3072
	ds_read_b128 v[142:145], v131
	ds_read_b128 v[138:141], v131 offset:1024
	ds_read_b128 v[134:137], v131 offset:2048
	ds_read_b128 v[130:133], v131 offset:3072
	s_mov_b64 s[70:71], s[62:63]
	v_mov_b32_e32 v205, v196
	s_mov_b32 m0, s1
	s_waitcnt lgkmcnt(0)
	ds_read_b128 v[162:165], v204 offset:32768
	ds_read_b128 v[166:169], v204 offset:33792
	ds_read_b128 v[170:173], v204 offset:34816
	ds_read_b128 v[174:177], v204 offset:35840
	ds_read_b128 v[178:181], v204 offset:36864
	ds_read_b128 v[182:185], v204 offset:37888
	ds_read_b128 v[186:189], v204 offset:38912
	ds_read_b128 v[190:193], v204 offset:39936
	s_add_u32 s62, s62, 0x40000
	global_load_lds_dwordx4 v205, s[70:71]
	v_mov_b32_e32 v205, v198
	s_mov_b32 m0, s23
	s_addc_u32 s63, s63, 0
	global_load_lds_dwordx4 v205, s[70:71]
	v_mov_b32_e32 v205, v196
	s_mov_b32 m0, s26
	s_nop 0
	global_load_lds_dwordx4 v205, s[62:63]
	v_mov_b32_e32 v205, v198
	s_mov_b32 m0, s27
	s_nop 0
	global_load_lds_dwordx4 v205, s[62:63]
	s_waitcnt vmcnt(8)
	s_waitcnt lgkmcnt(0)
	s_barrier
	s_setprio 1
	s_waitcnt lgkmcnt(0)
	v_mfma_i32_16x16x64_i8 v[18:21], v[158:161], v[162:165], v[18:21]
	s_nop 0
	v_mfma_i32_16x16x64_i8 v[18:21], v[154:157], v[166:169], v[18:21]
	v_mfma_i32_16x16x64_i8 v[22:25], v[150:153], v[162:165], v[22:25]
	s_nop 0
	v_mfma_i32_16x16x64_i8 v[22:25], v[146:149], v[166:169], v[22:25]
	v_mfma_i32_16x16x64_i8 v[26:29], v[142:145], v[162:165], v[26:29]
	s_nop 0
	v_mfma_i32_16x16x64_i8 v[26:29], v[138:141], v[166:169], v[26:29]
	v_mfma_i32_16x16x64_i8 v[34:37], v[134:137], v[162:165], v[34:37]
	s_nop 0
	v_mfma_i32_16x16x64_i8 v[34:37], v[130:133], v[166:169], v[34:37]
	v_mfma_i32_16x16x64_i8 v[50:53], v[158:161], v[170:173], v[50:53]
	s_nop 0
	v_mfma_i32_16x16x64_i8 v[50:53], v[154:157], v[174:177], v[50:53]
	v_mfma_i32_16x16x64_i8 v[62:65], v[150:153], v[170:173], v[62:65]
	s_nop 0
	v_mfma_i32_16x16x64_i8 v[62:65], v[146:149], v[174:177], v[62:65]
	v_mfma_i32_16x16x64_i8 v[54:57], v[142:145], v[170:173], v[54:57]
	s_nop 0
	v_mfma_i32_16x16x64_i8 v[54:57], v[138:141], v[174:177], v[54:57]
	v_mfma_i32_16x16x64_i8 v[66:69], v[134:137], v[170:173], v[66:69]
	s_nop 0
	v_mfma_i32_16x16x64_i8 v[66:69], v[130:133], v[174:177], v[66:69]
	v_mfma_i32_16x16x64_i8 v[82:85], v[158:161], v[178:181], v[82:85]
	s_nop 0
	v_mfma_i32_16x16x64_i8 v[82:85], v[154:157], v[182:185], v[82:85]
	v_mfma_i32_16x16x64_i8 v[94:97], v[150:153], v[178:181], v[94:97]
	s_nop 0
	v_mfma_i32_16x16x64_i8 v[94:97], v[146:149], v[182:185], v[94:97]
	v_mfma_i32_16x16x64_i8 v[86:89], v[142:145], v[178:181], v[86:89]
	s_nop 0
	v_mfma_i32_16x16x64_i8 v[86:89], v[138:141], v[182:185], v[86:89]
	v_mfma_i32_16x16x64_i8 v[98:101], v[134:137], v[178:181], v[98:101]
	s_nop 0
	v_mfma_i32_16x16x64_i8 v[98:101], v[130:133], v[182:185], v[98:101]
	v_mfma_i32_16x16x64_i8 v[114:117], v[158:161], v[186:189], v[114:117]
	s_nop 0
	v_mfma_i32_16x16x64_i8 v[114:117], v[154:157], v[190:193], v[114:117]
	v_mfma_i32_16x16x64_i8 v[122:125], v[150:153], v[186:189], v[122:125]
	s_nop 0
	v_mfma_i32_16x16x64_i8 v[122:125], v[146:149], v[190:193], v[122:125]
	v_mfma_i32_16x16x64_i8 v[118:121], v[142:145], v[186:189], v[118:121]
	s_nop 0
	v_mfma_i32_16x16x64_i8 v[118:121], v[138:141], v[190:193], v[118:121]
	v_mfma_i32_16x16x64_i8 v[126:129], v[134:137], v[186:189], v[126:129]
	s_nop 0
	v_mfma_i32_16x16x64_i8 v[126:129], v[130:133], v[190:193], v[126:129]
	s_setprio 0
	s_barrier
	v_mov_b32_e32 v205, v197
	s_add_i32 s51, s51, s10
	ds_read_b128 v[162:165], v204 offset:49152
	ds_read_b128 v[166:169], v204 offset:50176
	ds_read_b128 v[170:173], v204 offset:51200
	ds_read_b128 v[174:177], v204 offset:52224
	ds_read_b128 v[178:181], v204 offset:53248
	ds_read_b128 v[182:185], v204 offset:54272
	ds_read_b128 v[186:189], v204 offset:55296
	ds_read_b128 v[190:193], v204 offset:56320
	s_mov_b32 m0, s51
	s_nop 0
	global_load_lds_dwordx4 v205, s[76:77]
	v_mov_b32_e32 v205, v199
	s_add_i32 m0, s51, 0x2000
	s_add_u32 s62, s78, 0x40080
	global_load_lds_dwordx4 v205, s[76:77]
	s_addc_u32 s63, s79, 0
	v_mov_b32_e32 v205, v197
	s_add_i32 s51, s69, s10
	s_mov_b32 m0, s51
	s_nop 0
	global_load_lds_dwordx4 v205, s[62:63]
	v_mov_b32_e32 v205, v199
	s_add_i32 m0, s51, 0x2000
	s_nop 0
	global_load_lds_dwordx4 v205, s[62:63]
	s_waitcnt vmcnt(6)
	s_waitcnt lgkmcnt(0)
	s_barrier
	s_setprio 1
	s_waitcnt lgkmcnt(0)
	v_mfma_i32_16x16x64_i8 v[2:5], v[158:161], v[162:165], v[2:5]
	s_nop 0
	v_mfma_i32_16x16x64_i8 v[2:5], v[154:157], v[166:169], v[2:5]
	v_mfma_i32_16x16x64_i8 v[6:9], v[150:153], v[162:165], v[6:9]
	s_nop 0
	v_mfma_i32_16x16x64_i8 v[6:9], v[146:149], v[166:169], v[6:9]
	v_mfma_i32_16x16x64_i8 v[10:13], v[142:145], v[162:165], v[10:13]
	s_nop 0
	v_mfma_i32_16x16x64_i8 v[10:13], v[138:141], v[166:169], v[10:13]
	v_mfma_i32_16x16x64_i8 v[14:17], v[134:137], v[162:165], v[14:17]
	s_nop 0
	v_mfma_i32_16x16x64_i8 v[14:17], v[130:133], v[166:169], v[14:17]
	v_mfma_i32_16x16x64_i8 v[30:33], v[158:161], v[170:173], v[30:33]
	s_nop 0
	v_mfma_i32_16x16x64_i8 v[30:33], v[154:157], v[174:177], v[30:33]
	v_mfma_i32_16x16x64_i8 v[42:45], v[150:153], v[170:173], v[42:45]
	s_nop 0
	v_mfma_i32_16x16x64_i8 v[42:45], v[146:149], v[174:177], v[42:45]
	v_mfma_i32_16x16x64_i8 v[38:41], v[142:145], v[170:173], v[38:41]
	s_nop 0
	v_mfma_i32_16x16x64_i8 v[38:41], v[138:141], v[174:177], v[38:41]
	v_mfma_i32_16x16x64_i8 v[46:49], v[134:137], v[170:173], v[46:49]
	s_nop 0
	v_mfma_i32_16x16x64_i8 v[46:49], v[130:133], v[174:177], v[46:49]
	v_mfma_i32_16x16x64_i8 v[58:61], v[158:161], v[178:181], v[58:61]
	s_nop 0
	v_mfma_i32_16x16x64_i8 v[58:61], v[154:157], v[182:185], v[58:61]
	v_mfma_i32_16x16x64_i8 v[74:77], v[150:153], v[178:181], v[74:77]
	s_nop 0
	v_mfma_i32_16x16x64_i8 v[74:77], v[146:149], v[182:185], v[74:77]
	v_mfma_i32_16x16x64_i8 v[70:73], v[142:145], v[178:181], v[70:73]
	s_nop 0
	v_mfma_i32_16x16x64_i8 v[70:73], v[138:141], v[182:185], v[70:73]
	v_mfma_i32_16x16x64_i8 v[78:81], v[134:137], v[178:181], v[78:81]
	s_nop 0
	v_mfma_i32_16x16x64_i8 v[78:81], v[130:133], v[182:185], v[78:81]
	v_mfma_i32_16x16x64_i8 v[90:93], v[158:161], v[186:189], v[90:93]
	s_nop 0
	v_mfma_i32_16x16x64_i8 v[90:93], v[154:157], v[190:193], v[90:93]
	v_mfma_i32_16x16x64_i8 v[106:109], v[150:153], v[186:189], v[106:109]
	s_nop 0
	v_mfma_i32_16x16x64_i8 v[106:109], v[146:149], v[190:193], v[106:109]
	v_mfma_i32_16x16x64_i8 v[102:105], v[142:145], v[186:189], v[102:105]
	s_nop 0
	v_mfma_i32_16x16x64_i8 v[102:105], v[138:141], v[190:193], v[102:105]
	v_mfma_i32_16x16x64_i8 v[110:113], v[134:137], v[186:189], v[110:113]
	s_nop 0
	v_mfma_i32_16x16x64_i8 v[110:113], v[130:133], v[190:193], v[110:113]
	s_setprio 0
	s_barrier
	s_add_i32 s49, s49, 2
	s_add_u32 s66, s66, 0x100
	s_addc_u32 s67, s67, 0
	s_cmp_gt_u32 s49, 13
	s_cbranch_scc1 .LBB0_541
	s_mov_b64 s[78:79], s[8:9]
	s_mov_b64 s[76:77], s[40:41]

.LBB0_543:
	v_lshl_or_b32 v152, s61, 8, v203
	v_lshl_add_u32 v146, s33, 8, v201
	v_ashrrev_i32_e32 v153, 31, v152
	v_ashrrev_i32_e32 v147, 31, v146
	s_nop 15
	s_nop 7
	v_lshl_add_u64 v[130:131], v[152:153], 2, s[6:7]
	v_lshl_add_u64 v[150:151], v[146:147], 2, s[38:39]
	v_mov_b32_e32 v154, v232
	v_mov_b32_e32 v142, v210
	v_mov_b32_e32 v143, v211
	v_mov_b32_e32 v144, v212
	v_mov_b32_e32 v145, v213
	v_mov_b32_e32 v138, v214
	v_mov_b32_e32 v139, v215
	v_mov_b32_e32 v140, v216
	v_mov_b32_e32 v141, v217
	v_mov_b32_e32 v134, v218
	v_mov_b32_e32 v135, v219
	v_mov_b32_e32 v136, v220
	v_mov_b32_e32 v137, v221
	s_nop 0
	v_mov_b32_e32 v130, v222
	v_mov_b32_e32 v131, v223
	v_mov_b32_e32 v132, v224
	v_mov_b32_e32 v133, v225
	v_cvt_f32_i32_e32 v157, v19
	v_cvt_f32_i32_e32 v156, v18
	v_cvt_f32_i32_e32 v159, v21
	v_cvt_f32_i32_e32 v158, v20
	v_cvt_f32_i32_e32 v161, v23
	v_cvt_f32_i32_e32 v160, v22
	v_cvt_f32_i32_e32 v163, v25
	v_cvt_f32_i32_e32 v162, v24
	v_cvt_f32_i32_e32 v165, v27
	v_cvt_f32_i32_e32 v164, v26
	v_cvt_f32_i32_e32 v167, v29
	v_cvt_f32_i32_e32 v166, v28
	v_cvt_f32_i32_e32 v169, v35
	v_cvt_f32_i32_e32 v168, v34
	v_cvt_f32_i32_e32 v171, v37
	v_cvt_f32_i32_e32 v170, v36
	v_mov_b64_e32 v[148:149], s[36:37]
	v_mad_i64_i32 v[172:173], s[2:3], v146, s31, v[148:149]
	v_or_b32_e32 v174, 16, v146
	v_lshlrev_b64 v[152:153], 1, v[152:153]
	v_ashrrev_i32_e32 v175, 31, v174
	v_lshl_add_u64 v[172:173], v[172:173], 0, v[152:153]
	v_lshl_add_u64 v[176:177], v[174:175], 2, s[38:39]
	v_mad_i64_i32 v[174:175], s[2:3], v174, s31, v[148:149]
	v_lshl_add_u64 v[174:175], v[174:175], 0, v[152:153]
	v_add_u32_e32 v147, 0x80, v146
	s_andn2_b64 vcc, exec, s[42:43]
	v_pk_mul_f32 v[178:179], v[142:143], v[154:155] op_sel_hi:[1,0]
	v_pk_mul_f32 v[180:181], v[144:145], v[154:155] op_sel_hi:[1,0]
	v_pk_mul_f32 v[182:183], v[138:139], v[154:155] op_sel_hi:[1,0]
	v_pk_mul_f32 v[184:185], v[140:141], v[154:155] op_sel_hi:[1,0]
	v_pk_mul_f32 v[186:187], v[134:135], v[154:155] op_sel_hi:[1,0]
	v_pk_mul_f32 v[188:189], v[136:137], v[154:155] op_sel_hi:[1,0]
	v_pk_mul_f32 v[190:191], v[130:131], v[154:155] op_sel_hi:[1,0]
	v_pk_mul_f32 v[154:155], v[132:133], v[154:155] op_sel_hi:[1,0]
	v_pk_mul_f32 v[158:159], v[180:181], v[158:159]
	v_pk_mul_f32 v[156:157], v[178:179], v[156:157]
	v_pk_mul_f32 v[162:163], v[184:185], v[162:163]
	v_pk_mul_f32 v[160:161], v[182:183], v[160:161]
	v_pk_mul_f32 v[166:167], v[188:189], v[166:167]
	v_pk_mul_f32 v[164:165], v[186:187], v[164:165]
	v_pk_mul_f32 v[170:171], v[154:155], v[170:171]
	v_pk_mul_f32 v[168:169], v[190:191], v[168:169]
	v_cvt_pk_bf16_f32 v154, v156, v157
	v_cvt_pk_bf16_f32 v155, v158, v159
	v_cvt_pk_bf16_f32 v156, v160, v161
	v_cvt_pk_bf16_f32 v157, v162, v163
	v_cvt_pk_bf16_f32 v158, v164, v165
	v_cvt_pk_bf16_f32 v159, v166, v167
	v_cvt_pk_bf16_f32 v160, v168, v169
	v_cvt_pk_bf16_f32 v161, v170, v171
	global_store_dwordx4 v[172:173], v[154:157], off
	global_store_dwordx4 v[172:173], v[158:161], off offset:256
	v_cvt_f32_i32_e32 v157, v51
	v_cvt_f32_i32_e32 v156, v50
	v_cvt_f32_i32_e32 v159, v53
	v_cvt_f32_i32_e32 v158, v52
	v_cvt_f32_i32_e32 v161, v63
	v_cvt_f32_i32_e32 v160, v62
	v_cvt_f32_i32_e32 v163, v65
	v_cvt_f32_i32_e32 v162, v64
	v_cvt_f32_i32_e32 v165, v55
	v_cvt_f32_i32_e32 v164, v54
	v_cvt_f32_i32_e32 v167, v57
	v_cvt_f32_i32_e32 v166, v56
	v_cvt_f32_i32_e32 v169, v67
	v_cvt_f32_i32_e32 v168, v66
	v_cvt_f32_i32_e32 v171, v69
	v_cvt_f32_i32_e32 v170, v68
	v_or_b32_e32 v172, 32, v146
	v_ashrrev_i32_e32 v173, 31, v172
	v_lshl_add_u64 v[176:177], v[172:173], 2, s[38:39]
	v_mad_i64_i32 v[172:173], s[2:3], v172, s31, v[148:149]
	v_lshl_add_u64 v[172:173], v[172:173], 0, v[152:153]
	v_mov_b32_e32 v154, v233
	v_pk_mul_f32 v[178:179], v[142:143], v[154:155] op_sel_hi:[1,0]
	v_pk_mul_f32 v[180:181], v[144:145], v[154:155] op_sel_hi:[1,0]
	v_pk_mul_f32 v[182:183], v[138:139], v[154:155] op_sel_hi:[1,0]
	v_pk_mul_f32 v[184:185], v[140:141], v[154:155] op_sel_hi:[1,0]
	v_pk_mul_f32 v[186:187], v[134:135], v[154:155] op_sel_hi:[1,0]
	v_pk_mul_f32 v[188:189], v[136:137], v[154:155] op_sel_hi:[1,0]
	v_pk_mul_f32 v[190:191], v[130:131], v[154:155] op_sel_hi:[1,0]
	v_pk_mul_f32 v[154:155], v[132:133], v[154:155] op_sel_hi:[1,0]
	v_pk_mul_f32 v[158:159], v[180:181], v[158:159]
	v_pk_mul_f32 v[156:157], v[178:179], v[156:157]
	v_pk_mul_f32 v[162:163], v[184:185], v[162:163]
	v_pk_mul_f32 v[160:161], v[182:183], v[160:161]
	v_pk_mul_f32 v[166:167], v[188:189], v[166:167]
	v_pk_mul_f32 v[164:165], v[186:187], v[164:165]
	v_pk_mul_f32 v[170:171], v[154:155], v[170:171]
	v_pk_mul_f32 v[168:169], v[190:191], v[168:169]
	v_cvt_pk_bf16_f32 v154, v156, v157
	v_cvt_pk_bf16_f32 v155, v158, v159
	v_cvt_pk_bf16_f32 v156, v160, v161
	v_cvt_pk_bf16_f32 v157, v162, v163
	v_cvt_pk_bf16_f32 v158, v164, v165
	v_cvt_pk_bf16_f32 v159, v166, v167
	v_cvt_pk_bf16_f32 v160, v168, v169
	v_cvt_pk_bf16_f32 v161, v170, v171
	global_store_dwordx4 v[174:175], v[154:157], off
	global_store_dwordx4 v[174:175], v[158:161], off offset:256
	v_cvt_f32_i32_e32 v157, v83
	v_cvt_f32_i32_e32 v156, v82
	v_cvt_f32_i32_e32 v159, v85
	v_cvt_f32_i32_e32 v158, v84
	v_cvt_f32_i32_e32 v161, v95
	v_cvt_f32_i32_e32 v160, v94
	v_cvt_f32_i32_e32 v163, v97
	v_cvt_f32_i32_e32 v162, v96
	v_cvt_f32_i32_e32 v165, v87
	v_cvt_f32_i32_e32 v164, v86
	v_cvt_f32_i32_e32 v167, v89
	v_cvt_f32_i32_e32 v166, v88
	v_cvt_f32_i32_e32 v169, v99
	v_cvt_f32_i32_e32 v168, v98
	v_cvt_f32_i32_e32 v171, v101
	v_cvt_f32_i32_e32 v170, v100
	v_or_b32_e32 v174, 48, v146
	v_ashrrev_i32_e32 v175, 31, v174
	v_lshl_add_u64 v[176:177], v[174:175], 2, s[38:39]
	v_mov_b32_e32 v154, v234
	v_pk_mul_f32 v[178:179], v[142:143], v[154:155] op_sel_hi:[1,0]
	v_pk_mul_f32 v[180:181], v[144:145], v[154:155] op_sel_hi:[1,0]
	v_pk_mul_f32 v[182:183], v[138:139], v[154:155] op_sel_hi:[1,0]
	v_pk_mul_f32 v[184:185], v[140:141], v[154:155] op_sel_hi:[1,0]
	v_pk_mul_f32 v[186:187], v[134:135], v[154:155] op_sel_hi:[1,0]
	v_pk_mul_f32 v[188:189], v[136:137], v[154:155] op_sel_hi:[1,0]
	v_pk_mul_f32 v[190:191], v[130:131], v[154:155] op_sel_hi:[1,0]
	v_pk_mul_f32 v[154:155], v[132:133], v[154:155] op_sel_hi:[1,0]
	v_pk_mul_f32 v[158:159], v[180:181], v[158:159]
	v_pk_mul_f32 v[156:157], v[178:179], v[156:157]
	v_pk_mul_f32 v[162:163], v[184:185], v[162:163]
	v_pk_mul_f32 v[160:161], v[182:183], v[160:161]
	v_pk_mul_f32 v[166:167], v[188:189], v[166:167]
	v_pk_mul_f32 v[164:165], v[186:187], v[164:165]
	v_pk_mul_f32 v[170:171], v[154:155], v[170:171]
	v_pk_mul_f32 v[168:169], v[190:191], v[168:169]
	v_cvt_pk_bf16_f32 v154, v156, v157
	v_cvt_pk_bf16_f32 v155, v158, v159
	v_cvt_pk_bf16_f32 v156, v160, v161
	v_cvt_pk_bf16_f32 v157, v162, v163
	v_cvt_pk_bf16_f32 v158, v164, v165
	v_cvt_pk_bf16_f32 v159, v166, v167
	v_cvt_pk_bf16_f32 v160, v168, v169
	v_cvt_pk_bf16_f32 v161, v170, v171
	global_store_dwordx4 v[172:173], v[154:157], off
	global_store_dwordx4 v[172:173], v[158:161], off offset:256
	v_cvt_f32_i32_e32 v157, v115
	v_cvt_f32_i32_e32 v156, v114
	v_cvt_f32_i32_e32 v159, v117
	v_cvt_f32_i32_e32 v158, v116
	v_cvt_f32_i32_e32 v161, v123
	v_cvt_f32_i32_e32 v160, v122
	v_cvt_f32_i32_e32 v163, v125
	v_cvt_f32_i32_e32 v162, v124
	v_cvt_f32_i32_e32 v165, v119
	v_cvt_f32_i32_e32 v164, v118
	v_cvt_f32_i32_e32 v167, v121
	v_cvt_f32_i32_e32 v166, v120
	v_cvt_f32_i32_e32 v169, v127
	v_cvt_f32_i32_e32 v168, v126
	v_cvt_f32_i32_e32 v171, v129
	v_cvt_f32_i32_e32 v170, v128
	v_mad_i64_i32 v[172:173], s[2:3], v174, s31, v[148:149]
	v_lshl_add_u64 v[172:173], v[172:173], 0, v[152:153]
	v_mov_b32_e32 v154, v235
	v_pk_mul_f32 v[174:175], v[142:143], v[154:155] op_sel_hi:[1,0]
	v_pk_mul_f32 v[176:177], v[144:145], v[154:155] op_sel_hi:[1,0]
	v_pk_mul_f32 v[178:179], v[138:139], v[154:155] op_sel_hi:[1,0]
	v_pk_mul_f32 v[180:181], v[140:141], v[154:155] op_sel_hi:[1,0]
	v_pk_mul_f32 v[182:183], v[134:135], v[154:155] op_sel_hi:[1,0]
	v_pk_mul_f32 v[184:185], v[136:137], v[154:155] op_sel_hi:[1,0]
	v_pk_mul_f32 v[186:187], v[130:131], v[154:155] op_sel_hi:[1,0]
	v_pk_mul_f32 v[154:155], v[132:133], v[154:155] op_sel_hi:[1,0]
	v_pk_mul_f32 v[158:159], v[176:177], v[158:159]
	v_pk_mul_f32 v[156:157], v[174:175], v[156:157]
	v_pk_mul_f32 v[162:163], v[180:181], v[162:163]
	v_pk_mul_f32 v[160:161], v[178:179], v[160:161]
	v_pk_mul_f32 v[166:167], v[184:185], v[166:167]
	v_pk_mul_f32 v[164:165], v[182:183], v[164:165]
	v_pk_mul_f32 v[170:171], v[154:155], v[170:171]
	v_pk_mul_f32 v[168:169], v[186:187], v[168:169]
	v_cvt_pk_bf16_f32 v154, v156, v157
	v_cvt_pk_bf16_f32 v155, v158, v159
	v_cvt_pk_bf16_f32 v156, v160, v161
	v_cvt_pk_bf16_f32 v157, v162, v163
	v_cvt_pk_bf16_f32 v158, v164, v165
	v_cvt_pk_bf16_f32 v159, v166, v167
	v_cvt_pk_bf16_f32 v160, v168, v169
	v_cvt_pk_bf16_f32 v161, v170, v171
	global_store_dwordx4 v[172:173], v[154:157], off
	global_store_dwordx4 v[172:173], v[158:161], off offset:256
	v_cvt_f32_i32_e32 v157, v3
	v_cvt_f32_i32_e32 v156, v2
	v_cvt_f32_i32_e32 v159, v5
	v_cvt_f32_i32_e32 v158, v4
	v_cvt_f32_i32_e32 v161, v7
	v_cvt_f32_i32_e32 v160, v6
	v_cvt_f32_i32_e32 v163, v9
	v_cvt_f32_i32_e32 v162, v8
	v_cvt_f32_i32_e32 v165, v11
	v_cvt_f32_i32_e32 v164, v10
	v_cvt_f32_i32_e32 v167, v13
	v_cvt_f32_i32_e32 v166, v12
	v_cvt_f32_i32_e32 v169, v15
	v_cvt_f32_i32_e32 v168, v14
	v_cvt_f32_i32_e32 v171, v17
	v_cvt_f32_i32_e32 v170, v16
	v_mad_i64_i32 v[172:173], s[2:3], v147, s31, v[148:149]
	v_lshl_add_u64 v[172:173], v[172:173], 0, v[152:153]
	v_add_u32_e32 v147, 0x90, v146
	v_mov_b32_e32 v154, v236
	v_pk_mul_f32 v[174:175], v[142:143], v[154:155] op_sel_hi:[1,0]
	v_pk_mul_f32 v[176:177], v[144:145], v[154:155] op_sel_hi:[1,0]
	v_pk_mul_f32 v[178:179], v[138:139], v[154:155] op_sel_hi:[1,0]
	v_pk_mul_f32 v[180:181], v[140:141], v[154:155] op_sel_hi:[1,0]
	v_pk_mul_f32 v[182:183], v[134:135], v[154:155] op_sel_hi:[1,0]
	v_pk_mul_f32 v[184:185], v[136:137], v[154:155] op_sel_hi:[1,0]
	v_pk_mul_f32 v[186:187], v[130:131], v[154:155] op_sel_hi:[1,0]
	v_pk_mul_f32 v[154:155], v[132:133], v[154:155] op_sel_hi:[1,0]
	v_pk_mul_f32 v[158:159], v[176:177], v[158:159]
	v_pk_mul_f32 v[156:157], v[174:175], v[156:157]
	v_pk_mul_f32 v[162:163], v[180:181], v[162:163]
	v_pk_mul_f32 v[160:161], v[178:179], v[160:161]
	v_pk_mul_f32 v[166:167], v[184:185], v[166:167]
	v_pk_mul_f32 v[164:165], v[182:183], v[164:165]
	v_pk_mul_f32 v[170:171], v[154:155], v[170:171]
	v_pk_mul_f32 v[168:169], v[186:187], v[168:169]
	v_cvt_pk_bf16_f32 v154, v156, v157
	v_cvt_pk_bf16_f32 v155, v158, v159
	v_cvt_pk_bf16_f32 v156, v160, v161
	v_cvt_pk_bf16_f32 v157, v162, v163
	v_cvt_pk_bf16_f32 v158, v164, v165
	v_cvt_pk_bf16_f32 v159, v166, v167
	v_cvt_pk_bf16_f32 v160, v168, v169
	v_cvt_pk_bf16_f32 v161, v170, v171
	global_store_dwordx4 v[172:173], v[154:157], off
	global_store_dwordx4 v[172:173], v[158:161], off offset:256
	v_cvt_f32_i32_e32 v157, v31
	v_cvt_f32_i32_e32 v156, v30
	v_cvt_f32_i32_e32 v159, v33
	v_cvt_f32_i32_e32 v158, v32
	v_cvt_f32_i32_e32 v161, v43
	v_cvt_f32_i32_e32 v160, v42
	v_cvt_f32_i32_e32 v163, v45
	v_cvt_f32_i32_e32 v162, v44
	v_cvt_f32_i32_e32 v165, v39
	v_cvt_f32_i32_e32 v164, v38
	v_cvt_f32_i32_e32 v167, v41
	v_cvt_f32_i32_e32 v166, v40
	v_cvt_f32_i32_e32 v169, v47
	v_cvt_f32_i32_e32 v168, v46
	v_cvt_f32_i32_e32 v171, v49
	v_cvt_f32_i32_e32 v170, v48
	v_mad_i64_i32 v[172:173], s[2:3], v147, s31, v[148:149]
	v_lshl_add_u64 v[172:173], v[172:173], 0, v[152:153]
	v_add_u32_e32 v147, 0xa0, v146
	v_add_u32_e32 v146, 0xb0, v146
	v_mov_b32_e32 v154, v237
	v_pk_mul_f32 v[174:175], v[142:143], v[154:155] op_sel_hi:[1,0]
	v_pk_mul_f32 v[176:177], v[144:145], v[154:155] op_sel_hi:[1,0]
	v_pk_mul_f32 v[178:179], v[138:139], v[154:155] op_sel_hi:[1,0]
	v_pk_mul_f32 v[180:181], v[140:141], v[154:155] op_sel_hi:[1,0]
	v_pk_mul_f32 v[182:183], v[134:135], v[154:155] op_sel_hi:[1,0]
	v_pk_mul_f32 v[184:185], v[136:137], v[154:155] op_sel_hi:[1,0]
	v_pk_mul_f32 v[186:187], v[130:131], v[154:155] op_sel_hi:[1,0]
	v_pk_mul_f32 v[154:155], v[132:133], v[154:155] op_sel_hi:[1,0]
	v_pk_mul_f32 v[158:159], v[176:177], v[158:159]
	v_pk_mul_f32 v[156:157], v[174:175], v[156:157]
	v_pk_mul_f32 v[162:163], v[180:181], v[162:163]
	v_pk_mul_f32 v[160:161], v[178:179], v[160:161]
	v_pk_mul_f32 v[166:167], v[184:185], v[166:167]
	v_pk_mul_f32 v[164:165], v[182:183], v[164:165]
	v_pk_mul_f32 v[170:171], v[154:155], v[170:171]
	v_pk_mul_f32 v[168:169], v[186:187], v[168:169]
	v_cvt_pk_bf16_f32 v154, v156, v157
	v_cvt_pk_bf16_f32 v155, v158, v159
	v_cvt_pk_bf16_f32 v156, v160, v161
	v_cvt_pk_bf16_f32 v157, v162, v163
	v_cvt_pk_bf16_f32 v158, v164, v165
	v_cvt_pk_bf16_f32 v159, v166, v167
	v_cvt_pk_bf16_f32 v160, v168, v169
	v_cvt_pk_bf16_f32 v161, v170, v171
	global_store_dwordx4 v[172:173], v[154:157], off
	global_store_dwordx4 v[172:173], v[158:161], off offset:256
	v_cvt_f32_i32_e32 v157, v59
	v_cvt_f32_i32_e32 v156, v58
	v_cvt_f32_i32_e32 v159, v61
	v_cvt_f32_i32_e32 v158, v60
	v_cvt_f32_i32_e32 v161, v75
	v_cvt_f32_i32_e32 v160, v74
	v_cvt_f32_i32_e32 v163, v77
	v_cvt_f32_i32_e32 v162, v76
	v_cvt_f32_i32_e32 v165, v71
	v_cvt_f32_i32_e32 v164, v70
	v_cvt_f32_i32_e32 v167, v73
	v_cvt_f32_i32_e32 v166, v72
	v_cvt_f32_i32_e32 v169, v79
	v_cvt_f32_i32_e32 v168, v78
	v_cvt_f32_i32_e32 v171, v81
	v_cvt_f32_i32_e32 v170, v80
	v_mad_i64_i32 v[172:173], s[2:3], v147, s31, v[148:149]
	v_lshl_add_u64 v[172:173], v[172:173], 0, v[152:153]
	v_mad_i64_i32 v[146:147], s[2:3], v146, s31, v[148:149]
	v_lshl_add_u64 v[146:147], v[146:147], 0, v[152:153]
	s_mov_b64 s[2:3], -1
	v_mov_b32_e32 v154, v238
	v_pk_mul_f32 v[174:175], v[142:143], v[154:155] op_sel_hi:[1,0]
	v_pk_mul_f32 v[176:177], v[144:145], v[154:155] op_sel_hi:[1,0]
	v_pk_mul_f32 v[178:179], v[138:139], v[154:155] op_sel_hi:[1,0]
	v_pk_mul_f32 v[180:181], v[140:141], v[154:155] op_sel_hi:[1,0]
	v_pk_mul_f32 v[182:183], v[134:135], v[154:155] op_sel_hi:[1,0]
	v_pk_mul_f32 v[184:185], v[136:137], v[154:155] op_sel_hi:[1,0]
	v_pk_mul_f32 v[186:187], v[130:131], v[154:155] op_sel_hi:[1,0]
	v_pk_mul_f32 v[154:155], v[132:133], v[154:155] op_sel_hi:[1,0]
	v_pk_mul_f32 v[158:159], v[176:177], v[158:159]
	v_pk_mul_f32 v[156:157], v[174:175], v[156:157]
	v_pk_mul_f32 v[162:163], v[180:181], v[162:163]
	v_pk_mul_f32 v[160:161], v[178:179], v[160:161]
	v_pk_mul_f32 v[166:167], v[184:185], v[166:167]
	v_pk_mul_f32 v[164:165], v[182:183], v[164:165]
	v_pk_mul_f32 v[170:171], v[154:155], v[170:171]
	v_pk_mul_f32 v[168:169], v[186:187], v[168:169]
	v_cvt_pk_bf16_f32 v154, v156, v157
	v_cvt_pk_bf16_f32 v155, v158, v159
	v_cvt_pk_bf16_f32 v156, v160, v161
	v_cvt_pk_bf16_f32 v157, v162, v163
	v_cvt_pk_bf16_f32 v158, v164, v165
	v_cvt_pk_bf16_f32 v159, v166, v167
	v_cvt_pk_bf16_f32 v160, v168, v169
	v_cvt_pk_bf16_f32 v161, v170, v171
	global_store_dwordx4 v[172:173], v[154:157], off
	global_store_dwordx4 v[172:173], v[158:161], off offset:256
	v_cvt_f32_i32_e32 v155, v91
	v_cvt_f32_i32_e32 v154, v90
	v_cvt_f32_i32_e32 v157, v93
	v_cvt_f32_i32_e32 v156, v92
	v_cvt_f32_i32_e32 v159, v107
	v_cvt_f32_i32_e32 v158, v106
	v_cvt_f32_i32_e32 v161, v109
	v_cvt_f32_i32_e32 v160, v108
	v_cvt_f32_i32_e32 v163, v103
	v_cvt_f32_i32_e32 v162, v102
	v_cvt_f32_i32_e32 v165, v105
	v_cvt_f32_i32_e32 v164, v104
	v_cvt_f32_i32_e32 v167, v111
	v_cvt_f32_i32_e32 v166, v110
	v_cvt_f32_i32_e32 v169, v113
	v_cvt_f32_i32_e32 v168, v112
	v_mov_b32_e32 v150, v239
	v_pk_mul_f32 v[142:143], v[142:143], v[150:151] op_sel_hi:[1,0]
	v_pk_mul_f32 v[144:145], v[144:145], v[150:151] op_sel_hi:[1,0]
	v_pk_mul_f32 v[138:139], v[138:139], v[150:151] op_sel_hi:[1,0]
	v_pk_mul_f32 v[140:141], v[140:141], v[150:151] op_sel_hi:[1,0]
	v_pk_mul_f32 v[134:135], v[134:135], v[150:151] op_sel_hi:[1,0]
	v_pk_mul_f32 v[136:137], v[136:137], v[150:151] op_sel_hi:[1,0]
	v_pk_mul_f32 v[130:131], v[130:131], v[150:151] op_sel_hi:[1,0]
	v_pk_mul_f32 v[132:133], v[132:133], v[150:151] op_sel_hi:[1,0]
	v_pk_mul_f32 v[144:145], v[144:145], v[156:157]
	v_pk_mul_f32 v[142:143], v[142:143], v[154:155]
	v_pk_mul_f32 v[140:141], v[140:141], v[160:161]
	v_pk_mul_f32 v[138:139], v[138:139], v[158:159]
	v_pk_mul_f32 v[136:137], v[136:137], v[164:165]
	v_pk_mul_f32 v[134:135], v[134:135], v[162:163]
	v_pk_mul_f32 v[148:149], v[132:133], v[168:169]
	v_pk_mul_f32 v[150:151], v[130:131], v[166:167]
	v_cvt_pk_bf16_f32 v130, v142, v143
	v_cvt_pk_bf16_f32 v131, v144, v145
	v_cvt_pk_bf16_f32 v132, v138, v139
	v_cvt_pk_bf16_f32 v133, v140, v141
	v_cvt_pk_bf16_f32 v134, v134, v135
	v_cvt_pk_bf16_f32 v135, v136, v137
	v_cvt_pk_bf16_f32 v136, v150, v151
	v_cvt_pk_bf16_f32 v137, v148, v149
	global_store_dwordx4 v[146:147], v[130:133], off
	global_store_dwordx4 v[146:147], v[134:137], off offset:256
	s_cbranch_vccnz .LBB0_525
	s_andn2_b64 vcc, exec, s[4:5]
	s_cbranch_vccnz .LBB0_524
	s_barrier
	s_branch .LBB0_524

.LBB0_847:
	v_add_u32_e32 v130, 0, v206
	v_add_u32_e32 v131, 0x10000, v130
	v_add_u32_e32 v130, 0x14000, v130
	ds_read_b128 v[158:161], v131
	ds_read_b128 v[154:157], v131 offset:1024
	ds_read_b128 v[150:153], v131 offset:2048
	ds_read_b128 v[142:145], v131 offset:3072
	ds_read_b128 v[146:149], v130
	ds_read_b128 v[138:141], v130 offset:1024
	ds_read_b128 v[134:137], v130 offset:2048
	ds_read_b128 v[130:133], v130 offset:3072
	s_add_u32 s45, s30, s50
	s_addc_u32 s80, s31, s51
	s_add_u32 s8, s45, 0x80
	s_addc_u32 s9, s80, 0
	v_mov_b32_e32 v209, v201
	ds_read_b128 v[190:193], v207
	ds_read_b128 v[186:189], v207 offset:1024
	ds_read_b128 v[182:185], v207 offset:2048
	ds_read_b128 v[178:181], v207 offset:3072
	ds_read_b128 v[174:177], v207 offset:4096
	ds_read_b128 v[170:173], v207 offset:5120
	ds_read_b128 v[166:169], v207 offset:6144
	ds_read_b128 v[162:165], v207 offset:7168
	s_add_i32 m0, s1, 0x8000
	s_nop 0
	global_load_lds_dwordx4 v209, s[8:9]
	v_mov_b32_e32 v209, v203
	s_add_i32 m0, s1, 0xa000
	s_nop 0
	global_load_lds_dwordx4 v209, s[8:9]
	s_add_u32 s8, s45, 0x40080
	s_addc_u32 s9, s80, 0
	v_mov_b32_e32 v209, v201
	s_add_i32 m0, s1, 0xc000
	s_nop 0
	global_load_lds_dwordx4 v209, s[8:9]
	v_mov_b32_e32 v209, v203
	s_add_i32 m0, s1, 0xe000
	s_cmp_lg_u32 s43, -2
	global_load_lds_dwordx4 v209, s[8:9]
	s_mul_i32 s100, s73, 0x100
	s_mov_b32 s101, 0
	v_lshl_add_u32 v240, s72, 8, v205
	v_ashrrev_i32_e32 v241, 31, v240
	v_lshl_add_u64 v[242:243], s[100:101], 2, v[194:195]
	v_lshl_add_u64 v[240:241], v[240:241], 2, s[38:39]
	global_load_dwordx4 v[210:213], v[242:243], off
	global_load_dwordx4 v[214:217], v[242:243], off offset:16
	global_load_dwordx4 v[218:221], v[242:243], off offset:528
	global_load_dwordx4 v[222:225], v[242:243], off offset:512
	global_load_dword v232, v[240:241], off
	global_load_dword v233, v[240:241], off offset:64
	global_load_dword v234, v[240:241], off offset:128
	global_load_dword v235, v[240:241], off offset:192
	global_load_dword v236, v[240:241], off offset:512
	global_load_dword v237, v[240:241], off offset:576
	global_load_dword v238, v[240:241], off offset:640
	global_load_dword v239, v[240:241], off offset:704
	s_cselect_b64 s[66:67], -1, 0
	s_and_b64 vcc, exec, s[66:67]
	s_cbranch_vccnz .LBB0_850
	s_mov_b64 s[28:29], 0
	s_andn2_b64 vcc, exec, s[2:3]
	s_mov_b64 s[8:9], s[40:41]
	s_mov_b64 s[26:27], s[30:31]
	s_cbranch_vccnz .LBB0_851
	s_mov_b64 s[28:29], -1
	s_mov_b64 s[8:9], s[48:49]
	s_mov_b64 s[26:27], s[46:47]
	s_mov_b32 s0, s44
	s_mov_b32 s70, s42
	s_branch .LBB0_851

.LBB0_851:
	s_waitcnt vmcnt(20)
	s_waitcnt lgkmcnt(0)
	s_barrier
	s_setprio 1
	v_mfma_i32_16x16x64_i8 v[18:21], v[158:161], v[190:193], 0
	s_nop 0
	v_mfma_i32_16x16x64_i8 v[18:21], v[154:157], v[186:189], v[18:21]
	v_mfma_i32_16x16x64_i8 v[22:25], v[150:153], v[190:193], 0
	s_nop 0
	v_mfma_i32_16x16x64_i8 v[22:25], v[142:145], v[186:189], v[22:25]
	v_mfma_i32_16x16x64_i8 v[26:29], v[146:149], v[190:193], 0
	s_nop 0
	v_mfma_i32_16x16x64_i8 v[26:29], v[138:141], v[186:189], v[26:29]
	v_mfma_i32_16x16x64_i8 v[34:37], v[134:137], v[190:193], 0
	s_nop 0
	v_mfma_i32_16x16x64_i8 v[34:37], v[130:133], v[186:189], v[34:37]
	v_mfma_i32_16x16x64_i8 v[50:53], v[158:161], v[182:185], 0
	s_nop 0
	v_mfma_i32_16x16x64_i8 v[50:53], v[154:157], v[178:181], v[50:53]
	v_mfma_i32_16x16x64_i8 v[62:65], v[150:153], v[182:185], 0
	s_nop 0
	v_mfma_i32_16x16x64_i8 v[62:65], v[142:145], v[178:181], v[62:65]
	v_mfma_i32_16x16x64_i8 v[54:57], v[146:149], v[182:185], 0
	s_nop 0
	v_mfma_i32_16x16x64_i8 v[54:57], v[138:141], v[178:181], v[54:57]
	v_mfma_i32_16x16x64_i8 v[66:69], v[134:137], v[182:185], 0
	s_nop 0
	v_mfma_i32_16x16x64_i8 v[66:69], v[130:133], v[178:181], v[66:69]
	v_mfma_i32_16x16x64_i8 v[82:85], v[158:161], v[174:177], 0
	s_nop 0
	v_mfma_i32_16x16x64_i8 v[82:85], v[154:157], v[170:173], v[82:85]
	v_mfma_i32_16x16x64_i8 v[94:97], v[150:153], v[174:177], 0
	s_nop 0
	v_mfma_i32_16x16x64_i8 v[94:97], v[142:145], v[170:173], v[94:97]
	v_mfma_i32_16x16x64_i8 v[86:89], v[146:149], v[174:177], 0
	s_nop 0
	v_mfma_i32_16x16x64_i8 v[86:89], v[138:141], v[170:173], v[86:89]
	v_mfma_i32_16x16x64_i8 v[98:101], v[134:137], v[174:177], 0
	s_nop 0
	v_mfma_i32_16x16x64_i8 v[98:101], v[130:133], v[170:173], v[98:101]
	v_mfma_i32_16x16x64_i8 v[114:117], v[158:161], v[166:169], 0
	s_nop 0
	v_mfma_i32_16x16x64_i8 v[114:117], v[154:157], v[162:165], v[114:117]
	v_mfma_i32_16x16x64_i8 v[122:125], v[150:153], v[166:169], 0
	s_nop 0
	v_mfma_i32_16x16x64_i8 v[122:125], v[142:145], v[162:165], v[122:125]
	v_mfma_i32_16x16x64_i8 v[118:121], v[146:149], v[166:169], 0
	s_nop 0
	v_mfma_i32_16x16x64_i8 v[118:121], v[138:141], v[162:165], v[118:121]
	v_mfma_i32_16x16x64_i8 v[126:129], v[134:137], v[166:169], 0
	s_nop 0
	v_mfma_i32_16x16x64_i8 v[126:129], v[130:133], v[162:165], v[126:129]
	s_setprio 0
	s_barrier
	s_add_u32 s81, s74, s50
	s_addc_u32 s82, s75, s51
	s_cmp_eq_u32 s43, 12
	s_cselect_b64 s[76:77], -1, 0
	s_and_b64 s[78:79], s[76:77], exec
	s_cselect_b32 s65, s65, s82
	s_cselect_b32 s64, s64, s81
	s_mov_b64 s[78:79], s[64:65]
	v_mov_b32_e32 v209, v202
	s_mov_b32 m0, s21
	s_waitcnt lgkmcnt(0)
	ds_read_b128 v[190:193], v207 offset:16384
	ds_read_b128 v[186:189], v207 offset:17408
	ds_read_b128 v[182:185], v207 offset:18432
	ds_read_b128 v[178:181], v207 offset:19456
	ds_read_b128 v[174:177], v207 offset:20480
	ds_read_b128 v[170:173], v207 offset:21504
	ds_read_b128 v[166:169], v207 offset:22528
	ds_read_b128 v[162:165], v207 offset:23552
	s_nop 0
	global_load_lds_dwordx4 v209, s[78:79]
	v_mov_b32_e32 v209, v204
	s_mov_b32 m0, s33
	s_nop 0
	global_load_lds_dwordx4 v209, s[78:79]
	s_add_u32 s78, s64, 0x40000
	s_addc_u32 s79, s65, 0
	v_mov_b32_e32 v209, v202
	s_mov_b32 m0, s35
	s_nop 0
	global_load_lds_dwordx4 v209, s[78:79]
	v_mov_b32_e32 v209, v204
	s_mov_b32 m0, s60
	s_nop 0
	global_load_lds_dwordx4 v209, s[78:79]
	s_waitcnt vmcnt(18)
	s_waitcnt lgkmcnt(0)
	s_barrier
	s_setprio 1
	v_mfma_i32_16x16x64_i8 v[2:5], v[158:161], v[190:193], 0
	s_nop 0
	v_mfma_i32_16x16x64_i8 v[2:5], v[154:157], v[186:189], v[2:5]
	v_mfma_i32_16x16x64_i8 v[6:9], v[150:153], v[190:193], 0
	s_nop 0
	v_mfma_i32_16x16x64_i8 v[6:9], v[142:145], v[186:189], v[6:9]
	v_mfma_i32_16x16x64_i8 v[10:13], v[146:149], v[190:193], 0
	s_nop 0
	v_mfma_i32_16x16x64_i8 v[10:13], v[138:141], v[186:189], v[10:13]
	v_mfma_i32_16x16x64_i8 v[14:17], v[134:137], v[190:193], 0
	s_nop 0
	v_mfma_i32_16x16x64_i8 v[14:17], v[130:133], v[186:189], v[14:17]
	v_mfma_i32_16x16x64_i8 v[30:33], v[158:161], v[182:185], 0
	s_nop 0
	v_mfma_i32_16x16x64_i8 v[30:33], v[154:157], v[178:181], v[30:33]
	v_mfma_i32_16x16x64_i8 v[42:45], v[150:153], v[182:185], 0
	s_nop 0
	v_mfma_i32_16x16x64_i8 v[42:45], v[142:145], v[178:181], v[42:45]
	v_mfma_i32_16x16x64_i8 v[38:41], v[146:149], v[182:185], 0
	s_nop 0
	v_mfma_i32_16x16x64_i8 v[38:41], v[138:141], v[178:181], v[38:41]
	v_mfma_i32_16x16x64_i8 v[46:49], v[134:137], v[182:185], 0
	s_nop 0
	v_mfma_i32_16x16x64_i8 v[46:49], v[130:133], v[178:181], v[46:49]
	v_mfma_i32_16x16x64_i8 v[58:61], v[158:161], v[174:177], 0
	s_nop 0
	v_mfma_i32_16x16x64_i8 v[58:61], v[154:157], v[170:173], v[58:61]
	v_mfma_i32_16x16x64_i8 v[74:77], v[150:153], v[174:177], 0
	s_nop 0
	v_mfma_i32_16x16x64_i8 v[74:77], v[142:145], v[170:173], v[74:77]
	v_mfma_i32_16x16x64_i8 v[70:73], v[146:149], v[174:177], 0
	s_nop 0
	v_mfma_i32_16x16x64_i8 v[70:73], v[138:141], v[170:173], v[70:73]
	v_mfma_i32_16x16x64_i8 v[78:81], v[134:137], v[174:177], 0
	s_nop 0
	v_mfma_i32_16x16x64_i8 v[78:81], v[130:133], v[170:173], v[78:81]
	v_mfma_i32_16x16x64_i8 v[90:93], v[158:161], v[166:169], 0
	s_nop 0
	v_mfma_i32_16x16x64_i8 v[90:93], v[154:157], v[162:165], v[90:93]
	v_mfma_i32_16x16x64_i8 v[106:109], v[150:153], v[166:169], 0
	s_nop 0
	v_mfma_i32_16x16x64_i8 v[106:109], v[142:145], v[162:165], v[106:109]
	v_mfma_i32_16x16x64_i8 v[102:105], v[146:149], v[166:169], 0
	s_nop 0
	v_mfma_i32_16x16x64_i8 v[102:105], v[138:141], v[162:165], v[102:105]
	v_mfma_i32_16x16x64_i8 v[110:113], v[134:137], v[166:169], 0
	s_nop 0
	v_mfma_i32_16x16x64_i8 v[110:113], v[130:133], v[162:165], v[110:113]
	s_setprio 0
	s_barrier
	s_add_u32 s45, s45, 0x100
	s_addc_u32 s78, s80, 0
	s_and_b64 s[66:67], s[76:77], exec
	s_cselect_b32 s67, s53, s78
	s_cselect_b32 s66, s52, s45
	s_add_u32 s52, s64, 0x80
	s_addc_u32 s53, s65, 0
	s_add_i32 s45, 0, 0x18000
	s_add_i32 s78, 0, 0x1c000
	v_add_u32_e32 v130, s45, v206
	v_add_u32_e32 v131, s78, v206
	ds_read_b128 v[158:161], v130
	ds_read_b128 v[154:157], v130 offset:1024
	ds_read_b128 v[150:153], v130 offset:2048
	ds_read_b128 v[146:149], v130 offset:3072
	ds_read_b128 v[142:145], v131
	ds_read_b128 v[138:141], v131 offset:1024
	ds_read_b128 v[134:137], v131 offset:2048
	ds_read_b128 v[130:133], v131 offset:3072
	s_mov_b64 s[76:77], s[66:67]
	v_mov_b32_e32 v209, v201
	s_mov_b32 m0, s1
	s_waitcnt lgkmcnt(0)
	ds_read_b128 v[162:165], v207 offset:32768
	ds_read_b128 v[166:169], v207 offset:33792
	ds_read_b128 v[170:173], v207 offset:34816
	ds_read_b128 v[174:177], v207 offset:35840
	ds_read_b128 v[178:181], v207 offset:36864
	ds_read_b128 v[182:185], v207 offset:37888
	ds_read_b128 v[186:189], v207 offset:38912
	ds_read_b128 v[190:193], v207 offset:39936
	s_add_u32 s66, s66, 0x40000
	global_load_lds_dwordx4 v209, s[76:77]
	v_mov_b32_e32 v209, v203
	s_mov_b32 m0, s61
	s_addc_u32 s67, s67, 0
	global_load_lds_dwordx4 v209, s[76:77]
	v_mov_b32_e32 v209, v201
	s_mov_b32 m0, s62
	s_nop 0
	global_load_lds_dwordx4 v209, s[66:67]
	v_mov_b32_e32 v209, v203
	s_mov_b32 m0, s63
	s_nop 0
	global_load_lds_dwordx4 v209, s[66:67]
	s_waitcnt vmcnt(8)
	s_waitcnt lgkmcnt(0)
	s_barrier
	s_setprio 1
	s_waitcnt lgkmcnt(0)
	v_mfma_i32_16x16x64_i8 v[18:21], v[158:161], v[162:165], v[18:21]
	s_nop 0
	v_mfma_i32_16x16x64_i8 v[18:21], v[154:157], v[166:169], v[18:21]
	v_mfma_i32_16x16x64_i8 v[22:25], v[150:153], v[162:165], v[22:25]
	s_nop 0
	v_mfma_i32_16x16x64_i8 v[22:25], v[146:149], v[166:169], v[22:25]
	v_mfma_i32_16x16x64_i8 v[26:29], v[142:145], v[162:165], v[26:29]
	s_nop 0
	v_mfma_i32_16x16x64_i8 v[26:29], v[138:141], v[166:169], v[26:29]
	v_mfma_i32_16x16x64_i8 v[34:37], v[134:137], v[162:165], v[34:37]
	s_nop 0
	v_mfma_i32_16x16x64_i8 v[34:37], v[130:133], v[166:169], v[34:37]
	v_mfma_i32_16x16x64_i8 v[50:53], v[158:161], v[170:173], v[50:53]
	s_nop 0
	v_mfma_i32_16x16x64_i8 v[50:53], v[154:157], v[174:177], v[50:53]
	v_mfma_i32_16x16x64_i8 v[62:65], v[150:153], v[170:173], v[62:65]
	s_nop 0
	v_mfma_i32_16x16x64_i8 v[62:65], v[146:149], v[174:177], v[62:65]
	v_mfma_i32_16x16x64_i8 v[54:57], v[142:145], v[170:173], v[54:57]
	s_nop 0
	v_mfma_i32_16x16x64_i8 v[54:57], v[138:141], v[174:177], v[54:57]
	v_mfma_i32_16x16x64_i8 v[66:69], v[134:137], v[170:173], v[66:69]
	s_nop 0
	v_mfma_i32_16x16x64_i8 v[66:69], v[130:133], v[174:177], v[66:69]
	v_mfma_i32_16x16x64_i8 v[82:85], v[158:161], v[178:181], v[82:85]
	s_nop 0
	v_mfma_i32_16x16x64_i8 v[82:85], v[154:157], v[182:185], v[82:85]
	v_mfma_i32_16x16x64_i8 v[94:97], v[150:153], v[178:181], v[94:97]
	s_nop 0
	v_mfma_i32_16x16x64_i8 v[94:97], v[146:149], v[182:185], v[94:97]
	v_mfma_i32_16x16x64_i8 v[86:89], v[142:145], v[178:181], v[86:89]
	s_nop 0
	v_mfma_i32_16x16x64_i8 v[86:89], v[138:141], v[182:185], v[86:89]
	v_mfma_i32_16x16x64_i8 v[98:101], v[134:137], v[178:181], v[98:101]
	s_nop 0
	v_mfma_i32_16x16x64_i8 v[98:101], v[130:133], v[182:185], v[98:101]
	v_mfma_i32_16x16x64_i8 v[114:117], v[158:161], v[186:189], v[114:117]
	s_nop 0
	v_mfma_i32_16x16x64_i8 v[114:117], v[154:157], v[190:193], v[114:117]
	v_mfma_i32_16x16x64_i8 v[122:125], v[150:153], v[186:189], v[122:125]
	s_nop 0
	v_mfma_i32_16x16x64_i8 v[122:125], v[146:149], v[190:193], v[122:125]
	v_mfma_i32_16x16x64_i8 v[118:121], v[142:145], v[186:189], v[118:121]
	s_nop 0
	v_mfma_i32_16x16x64_i8 v[118:121], v[138:141], v[190:193], v[118:121]
	v_mfma_i32_16x16x64_i8 v[126:129], v[134:137], v[186:189], v[126:129]
	s_nop 0
	v_mfma_i32_16x16x64_i8 v[126:129], v[130:133], v[190:193], v[126:129]
	s_setprio 0
	s_barrier
	v_mov_b32_e32 v209, v202
	s_add_i32 s45, s45, s10
	ds_read_b128 v[162:165], v207 offset:49152
	ds_read_b128 v[166:169], v207 offset:50176
	ds_read_b128 v[170:173], v207 offset:51200
	ds_read_b128 v[174:177], v207 offset:52224
	ds_read_b128 v[178:181], v207 offset:53248
	ds_read_b128 v[182:185], v207 offset:54272
	ds_read_b128 v[186:189], v207 offset:55296
	ds_read_b128 v[190:193], v207 offset:56320
	s_mov_b32 m0, s45
	s_nop 0
	global_load_lds_dwordx4 v209, s[52:53]
	v_mov_b32_e32 v209, v204
	s_add_i32 m0, s45, 0x2000
	s_nop 0
	global_load_lds_dwordx4 v209, s[52:53]
	s_add_u32 s52, s64, 0x40080
	s_addc_u32 s53, s65, 0
	v_mov_b32_e32 v209, v202
	s_add_i32 s45, s78, s10
	s_mov_b32 m0, s45
	s_nop 0
	global_load_lds_dwordx4 v209, s[52:53]
	v_mov_b32_e32 v209, v204
	s_add_i32 m0, s45, 0x2000
	s_nop 0
	global_load_lds_dwordx4 v209, s[52:53]
	s_waitcnt vmcnt(6)
	s_waitcnt lgkmcnt(0)
	s_barrier
	s_setprio 1
	s_waitcnt lgkmcnt(0)
	v_mfma_i32_16x16x64_i8 v[2:5], v[158:161], v[162:165], v[2:5]
	s_nop 0
	v_mfma_i32_16x16x64_i8 v[2:5], v[154:157], v[166:169], v[2:5]
	v_mfma_i32_16x16x64_i8 v[6:9], v[150:153], v[162:165], v[6:9]
	s_nop 0
	v_mfma_i32_16x16x64_i8 v[6:9], v[146:149], v[166:169], v[6:9]
	v_mfma_i32_16x16x64_i8 v[10:13], v[142:145], v[162:165], v[10:13]
	s_nop 0
	v_mfma_i32_16x16x64_i8 v[10:13], v[138:141], v[166:169], v[10:13]
	v_mfma_i32_16x16x64_i8 v[14:17], v[134:137], v[162:165], v[14:17]
	s_nop 0
	v_mfma_i32_16x16x64_i8 v[14:17], v[130:133], v[166:169], v[14:17]
	v_mfma_i32_16x16x64_i8 v[30:33], v[158:161], v[170:173], v[30:33]
	s_nop 0
	v_mfma_i32_16x16x64_i8 v[30:33], v[154:157], v[174:177], v[30:33]
	v_mfma_i32_16x16x64_i8 v[42:45], v[150:153], v[170:173], v[42:45]
	s_nop 0
	v_mfma_i32_16x16x64_i8 v[42:45], v[146:149], v[174:177], v[42:45]
	v_mfma_i32_16x16x64_i8 v[38:41], v[142:145], v[170:173], v[38:41]
	s_nop 0
	v_mfma_i32_16x16x64_i8 v[38:41], v[138:141], v[174:177], v[38:41]
	v_mfma_i32_16x16x64_i8 v[46:49], v[134:137], v[170:173], v[46:49]
	s_nop 0
	v_mfma_i32_16x16x64_i8 v[46:49], v[130:133], v[174:177], v[46:49]
	v_mfma_i32_16x16x64_i8 v[58:61], v[158:161], v[178:181], v[58:61]
	s_nop 0
	v_mfma_i32_16x16x64_i8 v[58:61], v[154:157], v[182:185], v[58:61]
	v_mfma_i32_16x16x64_i8 v[74:77], v[150:153], v[178:181], v[74:77]
	s_nop 0
	v_mfma_i32_16x16x64_i8 v[74:77], v[146:149], v[182:185], v[74:77]
	v_mfma_i32_16x16x64_i8 v[70:73], v[142:145], v[178:181], v[70:73]
	s_nop 0
	v_mfma_i32_16x16x64_i8 v[70:73], v[138:141], v[182:185], v[70:73]
	v_mfma_i32_16x16x64_i8 v[78:81], v[134:137], v[178:181], v[78:81]
	s_nop 0
	v_mfma_i32_16x16x64_i8 v[78:81], v[130:133], v[182:185], v[78:81]
	v_mfma_i32_16x16x64_i8 v[90:93], v[158:161], v[186:189], v[90:93]
	s_nop 0
	v_mfma_i32_16x16x64_i8 v[90:93], v[154:157], v[190:193], v[90:93]
	v_mfma_i32_16x16x64_i8 v[106:109], v[150:153], v[186:189], v[106:109]
	s_nop 0
	v_mfma_i32_16x16x64_i8 v[106:109], v[146:149], v[190:193], v[106:109]
	v_mfma_i32_16x16x64_i8 v[102:105], v[142:145], v[186:189], v[102:105]
	s_nop 0
	v_mfma_i32_16x16x64_i8 v[102:105], v[138:141], v[190:193], v[102:105]
	v_mfma_i32_16x16x64_i8 v[110:113], v[134:137], v[186:189], v[110:113]
	s_nop 0
	v_mfma_i32_16x16x64_i8 v[110:113], v[130:133], v[190:193], v[110:113]
	s_setprio 0
	s_barrier
	s_add_i32 s43, s43, 2
	s_add_u32 s50, s50, 0x100
	s_addc_u32 s51, s51, 0
	s_cmp_gt_u32 s43, 13
	s_cbranch_scc1 .LBB0_861
	s_mov_b64 s[64:65], s[8:9]
	s_mov_b64 s[52:53], s[26:27]

.LBB0_863:
	s_lshl_b32 s2, s73, 8
	v_lshl_add_u32 v146, s72, 8, v205
	s_ashr_i32 s3, s2, 31
	v_ashrrev_i32_e32 v147, 31, v146
	s_nop 15
	s_nop 7
	v_lshl_add_u64 v[138:139], s[2:3], 2, v[194:195]
	v_lshl_add_u64 v[146:147], v[146:147], 2, s[38:39]
	v_mov_b32_e32 v142, v210
	v_mov_b32_e32 v143, v211
	v_mov_b32_e32 v144, v212
	v_mov_b32_e32 v145, v213
	v_mov_b32_e32 v134, v214
	v_mov_b32_e32 v135, v215
	v_mov_b32_e32 v136, v216
	v_mov_b32_e32 v137, v217
	v_mov_b32_e32 v130, v218
	v_mov_b32_e32 v131, v219
	v_mov_b32_e32 v132, v220
	v_mov_b32_e32 v133, v221
	s_nop 0
	v_mov_b32_e32 v138, v222
	v_mov_b32_e32 v139, v223
	v_mov_b32_e32 v140, v224
	v_mov_b32_e32 v141, v225
	v_cvt_f32_i32_e32 v149, v19
	v_mov_b32_e32 v167, v232
	v_cvt_f32_i32_e32 v148, v18
	v_cvt_f32_i32_e32 v151, v21
	v_cvt_f32_i32_e32 v150, v20
	v_cvt_f32_i32_e32 v153, v23
	v_cvt_f32_i32_e32 v152, v22
	v_cvt_f32_i32_e32 v155, v25
	v_cvt_f32_i32_e32 v154, v24
	v_cvt_f32_i32_e32 v157, v27
	v_cvt_f32_i32_e32 v156, v26
	v_cvt_f32_i32_e32 v159, v29
	v_cvt_f32_i32_e32 v158, v28
	v_cvt_f32_i32_e32 v163, v37
	v_cvt_f32_i32_e32 v162, v36
	v_cvt_f32_i32_e32 v161, v35
	v_cvt_f32_i32_e32 v160, v34
	v_mov_b32_e32 v164, 0
	v_mov_b32_e32 v165, 0
	s_mul_i32 s2, s72, 0x58
	s_add_i32 s2, s2, s73
	s_ashr_i32 s3, s2, 31
	v_pk_mul_f32 v[150:151], v[144:145], v[150:151]
	v_pk_mul_f32 v[148:149], v[142:143], v[148:149]
	v_pk_mul_f32 v[154:155], v[136:137], v[154:155]
	v_pk_mul_f32 v[152:153], v[134:135], v[152:153]
	v_pk_mul_f32 v[158:159], v[140:141], v[158:159]
	v_mul_f32_e32 v166, 0xbfb8aa3b, v167
	v_mul_f32_e32 v167, v167, v167
	v_pk_mul_f32 v[156:157], v[138:139], v[156:157]
	v_pk_mul_f32 v[162:163], v[132:133], v[162:163]
	v_div_scale_f32 v170, s[30:31], v167, v167, 1.0
	v_pk_mul_f32 v[168:169], v[148:149], v[166:167] op_sel_hi:[1,0]
	v_pk_mul_f32 v[158:159], v[150:151], v[158:159]
	v_pk_mul_f32 v[148:149], v[148:149], v[156:157]
	v_pk_mul_f32 v[150:151], v[150:151], v[166:167] op_sel_hi:[1,0]
	v_pk_mul_f32 v[156:157], v[152:153], v[166:167] op_sel_hi:[1,0]
	v_pk_mul_f32 v[162:163], v[154:155], v[162:163]
	v_pk_mul_f32 v[154:155], v[154:155], v[166:167] op_sel_hi:[1,0]
	v_rcp_f32_e32 v166, v170
	v_pk_mul_f32 v[160:161], v[130:131], v[160:161]
	v_div_scale_f32 v171, vcc, 1.0, v167, 1.0
	v_pk_mul_f32 v[152:153], v[152:153], v[160:161]
	v_exp_f32_e32 v160, v168
	v_fma_f32 v168, -v170, v166, 1.0
	v_fmac_f32_e32 v166, v168, v166
	v_mul_f32_e32 v168, v171, v166
	v_exp_f32_e32 v161, v169
	v_fma_f32 v169, -v170, v168, v171
	v_exp_f32_e32 v156, v156
	v_exp_f32_e32 v157, v157
	v_fmac_f32_e32 v168, v169, v166
	v_fma_f32 v169, -v170, v168, v171
	v_div_fmas_f32 v166, v169, v166, v168
	v_div_fixup_f32 v166, v166, v167, 1.0
	v_exp_f32_e32 v150, v150
	v_exp_f32_e32 v151, v151
	v_exp_f32_e32 v154, v154
	v_exp_f32_e32 v155, v155
	v_pk_fma_f32 v[160:161], v[166:167], v[160:161], v[166:167] op_sel_hi:[0,1,0]
	v_pk_fma_f32 v[156:157], v[166:167], v[156:157], v[166:167] op_sel_hi:[0,1,0]
	v_rcp_f32_e32 v160, v160
	v_rcp_f32_e32 v161, v161
	v_rcp_f32_e32 v156, v156
	v_rcp_f32_e32 v157, v157
	v_pk_fma_f32 v[150:151], v[166:167], v[150:151], v[166:167] op_sel_hi:[0,1,0]
	v_pk_fma_f32 v[154:155], v[166:167], v[154:155], v[166:167] op_sel_hi:[0,1,0]
	v_rcp_f32_e32 v150, v150
	v_rcp_f32_e32 v151, v151
	v_rcp_f32_e32 v154, v154
	v_rcp_f32_e32 v155, v155
	v_pk_mul_f32 v[148:149], v[148:149], v[160:161]
	v_pk_mul_f32 v[152:153], v[152:153], v[156:157]
	v_med3_f32 v148, v148, s6, v208
	v_med3_f32 v149, v149, s6, v208
	v_med3_f32 v152, v152, s6, v208
	v_med3_f32 v153, v153, s6, v208
	v_cvt_pk_fp8_f32 v164, v148, v149
	v_cvt_pk_fp8_f32 v165, v152, v153
	v_pk_mul_f32 v[150:151], v[158:159], v[150:151]
	v_pk_mul_f32 v[154:155], v[162:163], v[154:155]
	v_med3_f32 v150, v150, s6, v208
	v_med3_f32 v151, v151, s6, v208
	v_med3_f32 v148, v154, s6, v208
	v_med3_f32 v149, v155, s6, v208
	v_cvt_pk_fp8_f32 v164, v150, v151 op_sel:[0,0,1]
	v_cvt_pk_fp8_f32 v165, v148, v149 op_sel:[0,0,1]
	s_lshl_b64 s[30:31], s[2:3], 14
	v_lshl_add_u64 v[148:149], v[196:197], 0, s[30:31]
	v_cvt_f32_i32_e32 v151, v51
	global_store_dwordx2 v[148:149], v[164:165], off
	v_cvt_f32_i32_e32 v150, v50
	v_cvt_f32_i32_e32 v153, v53
	v_cvt_f32_i32_e32 v152, v52
	v_cvt_f32_i32_e32 v155, v63
	v_cvt_f32_i32_e32 v154, v62
	v_cvt_f32_i32_e32 v157, v65
	v_cvt_f32_i32_e32 v156, v64
	v_cvt_f32_i32_e32 v159, v55
	v_cvt_f32_i32_e32 v158, v54
	v_cvt_f32_i32_e32 v161, v57
	v_cvt_f32_i32_e32 v160, v56
	v_cvt_f32_i32_e32 v163, v67
	v_cvt_f32_i32_e32 v162, v66
	v_cvt_f32_i32_e32 v165, v69
	v_cvt_f32_i32_e32 v164, v68
	v_pk_mul_f32 v[152:153], v[144:145], v[152:153]
	v_pk_mul_f32 v[150:151], v[142:143], v[150:151]
	v_pk_mul_f32 v[156:157], v[136:137], v[156:157]
	v_pk_mul_f32 v[154:155], v[134:135], v[154:155]
	v_pk_mul_f32 v[160:161], v[140:141], v[160:161]
	v_pk_mul_f32 v[158:159], v[138:139], v[158:159]
	v_pk_mul_f32 v[164:165], v[132:133], v[164:165]
	v_pk_mul_f32 v[162:163], v[130:131], v[162:163]
	v_pk_mul_f32 v[160:161], v[152:153], v[160:161]
	v_pk_mul_f32 v[158:159], v[150:151], v[158:159]
	v_pk_mul_f32 v[164:165], v[156:157], v[164:165]
	v_pk_mul_f32 v[162:163], v[154:155], v[162:163]
	v_mov_b32_e32 v166, 0
	v_mov_b32_e32 v167, 0
	s_add_i32 s2, s2, 44
	s_ashr_i32 s3, s2, 31
	s_lshl_b64 s[2:3], s[2:3], 14
	v_mov_b32_e32 v169, v233
	v_mul_f32_e32 v168, 0xbfb8aa3b, v169
	v_mul_f32_e32 v169, v169, v169
	v_div_scale_f32 v170, s[30:31], v169, v169, 1.0
	v_pk_mul_f32 v[150:151], v[150:151], v[168:169] op_sel_hi:[1,0]
	v_pk_mul_f32 v[152:153], v[152:153], v[168:169] op_sel_hi:[1,0]
	v_pk_mul_f32 v[154:155], v[154:155], v[168:169] op_sel_hi:[1,0]
	v_pk_mul_f32 v[156:157], v[156:157], v[168:169] op_sel_hi:[1,0]
	v_rcp_f32_e32 v168, v170
	v_div_scale_f32 v171, vcc, 1.0, v169, 1.0
	v_exp_f32_e32 v150, v150
	v_fma_f32 v172, -v170, v168, 1.0
	v_fmac_f32_e32 v168, v172, v168
	v_mul_f32_e32 v172, v171, v168
	v_fma_f32 v173, -v170, v172, v171
	v_exp_f32_e32 v151, v151
	v_exp_f32_e32 v154, v154
	v_exp_f32_e32 v155, v155
	v_fmac_f32_e32 v172, v173, v168
	v_fma_f32 v170, -v170, v172, v171
	v_div_fmas_f32 v168, v170, v168, v172
	v_div_fixup_f32 v168, v168, v169, 1.0
	v_exp_f32_e32 v152, v152
	v_exp_f32_e32 v153, v153
	v_exp_f32_e32 v156, v156
	v_exp_f32_e32 v157, v157
	v_pk_fma_f32 v[150:151], v[168:169], v[150:151], v[168:169] op_sel_hi:[0,1,0]
	v_pk_fma_f32 v[154:155], v[168:169], v[154:155], v[168:169] op_sel_hi:[0,1,0]
	v_rcp_f32_e32 v150, v150
	v_rcp_f32_e32 v151, v151
	v_rcp_f32_e32 v154, v154
	v_rcp_f32_e32 v155, v155
	v_pk_fma_f32 v[152:153], v[168:169], v[152:153], v[168:169] op_sel_hi:[0,1,0]
	v_pk_fma_f32 v[156:157], v[168:169], v[156:157], v[168:169] op_sel_hi:[0,1,0]
	v_rcp_f32_e32 v152, v152
	v_rcp_f32_e32 v153, v153
	v_rcp_f32_e32 v156, v156
	v_rcp_f32_e32 v157, v157
	v_pk_mul_f32 v[150:151], v[158:159], v[150:151]
	v_pk_mul_f32 v[154:155], v[162:163], v[154:155]
	v_med3_f32 v150, v150, s6, v208
	v_med3_f32 v151, v151, s6, v208
	v_med3_f32 v154, v154, s6, v208
	v_med3_f32 v155, v155, s6, v208
	v_cvt_pk_fp8_f32 v166, v150, v151
	v_cvt_pk_fp8_f32 v167, v154, v155
	v_pk_mul_f32 v[152:153], v[160:161], v[152:153]
	v_pk_mul_f32 v[156:157], v[164:165], v[156:157]
	v_med3_f32 v152, v152, s6, v208
	v_med3_f32 v153, v153, s6, v208
	v_med3_f32 v150, v156, s6, v208
	v_med3_f32 v151, v157, s6, v208
	v_cvt_pk_fp8_f32 v166, v152, v153 op_sel:[0,0,1]
	v_cvt_pk_fp8_f32 v167, v150, v151 op_sel:[0,0,1]
	v_cvt_f32_i32_e32 v151, v83
	v_cvt_f32_i32_e32 v150, v82
	v_cvt_f32_i32_e32 v153, v85
	global_store_dwordx2 v[148:149], v[166:167], off offset:2048
	v_cvt_f32_i32_e32 v152, v84
	v_cvt_f32_i32_e32 v155, v95
	v_cvt_f32_i32_e32 v154, v94
	v_cvt_f32_i32_e32 v157, v97
	v_cvt_f32_i32_e32 v156, v96
	v_cvt_f32_i32_e32 v159, v87
	v_cvt_f32_i32_e32 v158, v86
	v_cvt_f32_i32_e32 v161, v89
	v_cvt_f32_i32_e32 v160, v88
	v_cvt_f32_i32_e32 v163, v99
	v_cvt_f32_i32_e32 v162, v98
	v_cvt_f32_i32_e32 v165, v101
	v_cvt_f32_i32_e32 v164, v100
	v_pk_mul_f32 v[152:153], v[144:145], v[152:153]
	v_pk_mul_f32 v[150:151], v[142:143], v[150:151]
	v_pk_mul_f32 v[156:157], v[136:137], v[156:157]
	v_pk_mul_f32 v[154:155], v[134:135], v[154:155]
	v_pk_mul_f32 v[160:161], v[140:141], v[160:161]
	v_pk_mul_f32 v[158:159], v[138:139], v[158:159]
	v_pk_mul_f32 v[164:165], v[132:133], v[164:165]
	v_pk_mul_f32 v[162:163], v[130:131], v[162:163]
	v_pk_mul_f32 v[160:161], v[152:153], v[160:161]
	v_pk_mul_f32 v[158:159], v[150:151], v[158:159]
	v_pk_mul_f32 v[164:165], v[156:157], v[164:165]
	v_pk_mul_f32 v[162:163], v[154:155], v[162:163]
	v_mov_b32_e32 v166, 0
	v_mov_b32_e32 v167, 0
	v_mov_b32_e32 v169, v234
	v_mul_f32_e32 v168, 0xbfb8aa3b, v169
	v_mul_f32_e32 v169, v169, v169
	v_div_scale_f32 v170, s[30:31], v169, v169, 1.0
	v_pk_mul_f32 v[150:151], v[150:151], v[168:169] op_sel_hi:[1,0]
	v_pk_mul_f32 v[152:153], v[152:153], v[168:169] op_sel_hi:[1,0]
	v_pk_mul_f32 v[154:155], v[154:155], v[168:169] op_sel_hi:[1,0]
	v_pk_mul_f32 v[156:157], v[156:157], v[168:169] op_sel_hi:[1,0]
	v_rcp_f32_e32 v168, v170
	v_div_scale_f32 v171, vcc, 1.0, v169, 1.0
	v_exp_f32_e32 v150, v150
	v_fma_f32 v172, -v170, v168, 1.0
	v_fmac_f32_e32 v168, v172, v168
	v_mul_f32_e32 v172, v171, v168
	v_fma_f32 v173, -v170, v172, v171
	v_exp_f32_e32 v151, v151
	v_exp_f32_e32 v154, v154
	v_exp_f32_e32 v155, v155
	v_fmac_f32_e32 v172, v173, v168
	v_fma_f32 v170, -v170, v172, v171
	v_div_fmas_f32 v168, v170, v168, v172
	v_div_fixup_f32 v168, v168, v169, 1.0
	v_exp_f32_e32 v152, v152
	v_exp_f32_e32 v153, v153
	v_exp_f32_e32 v156, v156
	v_exp_f32_e32 v157, v157
	v_pk_fma_f32 v[150:151], v[168:169], v[150:151], v[168:169] op_sel_hi:[0,1,0]
	v_pk_fma_f32 v[154:155], v[168:169], v[154:155], v[168:169] op_sel_hi:[0,1,0]
	v_rcp_f32_e32 v150, v150
	v_rcp_f32_e32 v151, v151
	v_rcp_f32_e32 v154, v154
	v_rcp_f32_e32 v155, v155
	v_pk_fma_f32 v[152:153], v[168:169], v[152:153], v[168:169] op_sel_hi:[0,1,0]
	v_pk_fma_f32 v[156:157], v[168:169], v[156:157], v[168:169] op_sel_hi:[0,1,0]
	v_rcp_f32_e32 v152, v152
	v_rcp_f32_e32 v153, v153
	v_rcp_f32_e32 v156, v156
	v_rcp_f32_e32 v157, v157
	v_pk_mul_f32 v[150:151], v[158:159], v[150:151]
	v_pk_mul_f32 v[154:155], v[162:163], v[154:155]
	v_med3_f32 v150, v150, s6, v208
	v_med3_f32 v151, v151, s6, v208
	v_med3_f32 v154, v154, s6, v208
	v_med3_f32 v155, v155, s6, v208
	v_cvt_pk_fp8_f32 v166, v150, v151
	v_cvt_pk_fp8_f32 v167, v154, v155
	v_pk_mul_f32 v[152:153], v[160:161], v[152:153]
	v_pk_mul_f32 v[156:157], v[164:165], v[156:157]
	v_med3_f32 v152, v152, s6, v208
	v_med3_f32 v153, v153, s6, v208
	v_med3_f32 v150, v156, s6, v208
	v_med3_f32 v151, v157, s6, v208
	v_cvt_pk_fp8_f32 v166, v152, v153 op_sel:[0,0,1]
	v_cvt_pk_fp8_f32 v167, v150, v151 op_sel:[0,0,1]
	v_add_co_u32_e32 v148, vcc, s71, v148
	v_cvt_f32_i32_e32 v151, v115
	s_nop 0
	v_addc_co_u32_e32 v149, vcc, 0, v149, vcc
	global_store_dwordx2 v[148:149], v[166:167], off
	v_cvt_f32_i32_e32 v150, v114
	v_cvt_f32_i32_e32 v153, v117
	v_cvt_f32_i32_e32 v152, v116
	v_cvt_f32_i32_e32 v155, v123
	v_cvt_f32_i32_e32 v154, v122
	v_cvt_f32_i32_e32 v157, v125
	v_cvt_f32_i32_e32 v156, v124
	v_cvt_f32_i32_e32 v159, v119
	v_cvt_f32_i32_e32 v158, v118
	v_cvt_f32_i32_e32 v161, v121
	v_cvt_f32_i32_e32 v160, v120
	v_cvt_f32_i32_e32 v163, v127
	v_cvt_f32_i32_e32 v162, v126
	v_cvt_f32_i32_e32 v165, v129
	v_cvt_f32_i32_e32 v164, v128
	v_pk_mul_f32 v[152:153], v[144:145], v[152:153]
	v_pk_mul_f32 v[150:151], v[142:143], v[150:151]
	v_pk_mul_f32 v[156:157], v[136:137], v[156:157]
	v_pk_mul_f32 v[154:155], v[134:135], v[154:155]
	v_pk_mul_f32 v[160:161], v[140:141], v[160:161]
	v_pk_mul_f32 v[158:159], v[138:139], v[158:159]
	v_pk_mul_f32 v[164:165], v[132:133], v[164:165]
	v_pk_mul_f32 v[162:163], v[130:131], v[162:163]
	v_pk_mul_f32 v[160:161], v[152:153], v[160:161]
	v_pk_mul_f32 v[158:159], v[150:151], v[158:159]
	v_pk_mul_f32 v[164:165], v[156:157], v[164:165]
	v_pk_mul_f32 v[162:163], v[154:155], v[162:163]
	v_mov_b32_e32 v166, 0
	v_mov_b32_e32 v167, 0
	v_mov_b32_e32 v169, v235
	v_mul_f32_e32 v168, 0xbfb8aa3b, v169
	v_mul_f32_e32 v169, v169, v169
	v_div_scale_f32 v170, s[30:31], v169, v169, 1.0
	v_pk_mul_f32 v[150:151], v[150:151], v[168:169] op_sel_hi:[1,0]
	v_pk_mul_f32 v[152:153], v[152:153], v[168:169] op_sel_hi:[1,0]
	v_pk_mul_f32 v[154:155], v[154:155], v[168:169] op_sel_hi:[1,0]
	v_pk_mul_f32 v[156:157], v[156:157], v[168:169] op_sel_hi:[1,0]
	v_rcp_f32_e32 v168, v170
	v_div_scale_f32 v171, vcc, 1.0, v169, 1.0
	v_exp_f32_e32 v150, v150
	v_fma_f32 v172, -v170, v168, 1.0
	v_fmac_f32_e32 v168, v172, v168
	v_mul_f32_e32 v172, v171, v168
	v_fma_f32 v173, -v170, v172, v171
	v_exp_f32_e32 v151, v151
	v_exp_f32_e32 v154, v154
	v_exp_f32_e32 v155, v155
	v_fmac_f32_e32 v172, v173, v168
	v_fma_f32 v170, -v170, v172, v171
	v_div_fmas_f32 v168, v170, v168, v172
	v_div_fixup_f32 v168, v168, v169, 1.0
	v_exp_f32_e32 v152, v152
	v_exp_f32_e32 v153, v153
	v_exp_f32_e32 v156, v156
	v_exp_f32_e32 v157, v157
	v_pk_fma_f32 v[150:151], v[168:169], v[150:151], v[168:169] op_sel_hi:[0,1,0]
	v_pk_fma_f32 v[154:155], v[168:169], v[154:155], v[168:169] op_sel_hi:[0,1,0]
	v_rcp_f32_e32 v150, v150
	v_rcp_f32_e32 v151, v151
	v_rcp_f32_e32 v154, v154
	v_rcp_f32_e32 v155, v155
	v_pk_fma_f32 v[152:153], v[168:169], v[152:153], v[168:169] op_sel_hi:[0,1,0]
	v_pk_fma_f32 v[156:157], v[168:169], v[156:157], v[168:169] op_sel_hi:[0,1,0]
	v_rcp_f32_e32 v152, v152
	v_rcp_f32_e32 v153, v153
	v_rcp_f32_e32 v156, v156
	v_rcp_f32_e32 v157, v157
	v_pk_mul_f32 v[150:151], v[158:159], v[150:151]
	v_pk_mul_f32 v[154:155], v[162:163], v[154:155]
	v_med3_f32 v150, v150, s6, v208
	v_med3_f32 v151, v151, s6, v208
	v_med3_f32 v154, v154, s6, v208
	v_med3_f32 v155, v155, s6, v208
	v_cvt_pk_fp8_f32 v166, v150, v151
	v_cvt_pk_fp8_f32 v167, v154, v155
	v_pk_mul_f32 v[152:153], v[160:161], v[152:153]
	v_pk_mul_f32 v[156:157], v[164:165], v[156:157]
	v_med3_f32 v152, v152, s6, v208
	v_med3_f32 v153, v153, s6, v208
	v_med3_f32 v150, v156, s6, v208
	v_med3_f32 v151, v157, s6, v208
	v_cvt_pk_fp8_f32 v166, v152, v153 op_sel:[0,0,1]
	v_cvt_pk_fp8_f32 v167, v150, v151 op_sel:[0,0,1]
	v_cvt_f32_i32_e32 v151, v5
	v_cvt_f32_i32_e32 v150, v4
	v_cvt_f32_i32_e32 v153, v7
	global_store_dwordx2 v[148:149], v[166:167], off offset:2048
	v_cvt_f32_i32_e32 v149, v3
	v_cvt_f32_i32_e32 v148, v2
	v_cvt_f32_i32_e32 v152, v6
	v_cvt_f32_i32_e32 v155, v9
	v_cvt_f32_i32_e32 v154, v8
	v_cvt_f32_i32_e32 v157, v11
	v_cvt_f32_i32_e32 v156, v10
	v_cvt_f32_i32_e32 v159, v13
	v_cvt_f32_i32_e32 v158, v12
	v_cvt_f32_i32_e32 v161, v15
	v_cvt_f32_i32_e32 v160, v14
	v_cvt_f32_i32_e32 v163, v17
	v_cvt_f32_i32_e32 v162, v16
	v_pk_mul_f32 v[150:151], v[144:145], v[150:151]
	v_pk_mul_f32 v[148:149], v[142:143], v[148:149]
	v_pk_mul_f32 v[154:155], v[136:137], v[154:155]
	v_pk_mul_f32 v[152:153], v[134:135], v[152:153]
	v_pk_mul_f32 v[158:159], v[140:141], v[158:159]
	v_pk_mul_f32 v[156:157], v[138:139], v[156:157]
	v_pk_mul_f32 v[162:163], v[132:133], v[162:163]
	v_pk_mul_f32 v[160:161], v[130:131], v[160:161]
	v_pk_mul_f32 v[158:159], v[150:151], v[158:159]
	v_pk_mul_f32 v[156:157], v[148:149], v[156:157]
	v_pk_mul_f32 v[162:163], v[154:155], v[162:163]
	v_pk_mul_f32 v[160:161], v[152:153], v[160:161]
	v_mov_b32_e32 v164, 0
	v_mov_b32_e32 v165, 0
	v_mov_b32_e32 v167, v236
	v_mul_f32_e32 v166, 0xbfb8aa3b, v167
	v_mul_f32_e32 v167, v167, v167
	v_div_scale_f32 v168, s[30:31], v167, v167, 1.0
	v_pk_mul_f32 v[148:149], v[148:149], v[166:167] op_sel_hi:[1,0]
	v_pk_mul_f32 v[150:151], v[150:151], v[166:167] op_sel_hi:[1,0]
	v_pk_mul_f32 v[152:153], v[152:153], v[166:167] op_sel_hi:[1,0]
	v_pk_mul_f32 v[154:155], v[154:155], v[166:167] op_sel_hi:[1,0]
	v_rcp_f32_e32 v166, v168
	v_div_scale_f32 v169, vcc, 1.0, v167, 1.0
	v_exp_f32_e32 v148, v148
	v_fma_f32 v170, -v168, v166, 1.0
	v_fmac_f32_e32 v166, v170, v166
	v_mul_f32_e32 v170, v169, v166
	v_fma_f32 v171, -v168, v170, v169
	v_exp_f32_e32 v149, v149
	v_exp_f32_e32 v152, v152
	v_exp_f32_e32 v153, v153
	v_fmac_f32_e32 v170, v171, v166
	v_fma_f32 v168, -v168, v170, v169
	v_div_fmas_f32 v166, v168, v166, v170
	v_div_fixup_f32 v166, v166, v167, 1.0
	v_exp_f32_e32 v150, v150
	v_exp_f32_e32 v151, v151
	v_exp_f32_e32 v154, v154
	v_exp_f32_e32 v155, v155
	v_pk_fma_f32 v[148:149], v[166:167], v[148:149], v[166:167] op_sel_hi:[0,1,0]
	v_pk_fma_f32 v[152:153], v[166:167], v[152:153], v[166:167] op_sel_hi:[0,1,0]
	v_rcp_f32_e32 v148, v148
	v_rcp_f32_e32 v149, v149
	v_rcp_f32_e32 v152, v152
	v_rcp_f32_e32 v153, v153
	v_pk_fma_f32 v[150:151], v[166:167], v[150:151], v[166:167] op_sel_hi:[0,1,0]
	v_pk_fma_f32 v[154:155], v[166:167], v[154:155], v[166:167] op_sel_hi:[0,1,0]
	v_rcp_f32_e32 v150, v150
	v_rcp_f32_e32 v151, v151
	v_rcp_f32_e32 v154, v154
	v_rcp_f32_e32 v155, v155
	v_pk_mul_f32 v[148:149], v[156:157], v[148:149]
	v_pk_mul_f32 v[152:153], v[160:161], v[152:153]
	v_med3_f32 v148, v148, s6, v208
	v_med3_f32 v149, v149, s6, v208
	v_med3_f32 v152, v152, s6, v208
	v_med3_f32 v153, v153, s6, v208
	v_cvt_pk_fp8_f32 v164, v148, v149
	v_cvt_pk_fp8_f32 v165, v152, v153
	v_pk_mul_f32 v[150:151], v[158:159], v[150:151]
	v_pk_mul_f32 v[154:155], v[162:163], v[154:155]
	v_med3_f32 v150, v150, s6, v208
	v_med3_f32 v151, v151, s6, v208
	v_med3_f32 v148, v154, s6, v208
	v_med3_f32 v149, v155, s6, v208
	v_cvt_pk_fp8_f32 v164, v150, v151 op_sel:[0,0,1]
	v_cvt_pk_fp8_f32 v165, v148, v149 op_sel:[0,0,1]
	v_lshl_add_u64 v[148:149], v[196:197], 0, s[2:3]
	v_cvt_f32_i32_e32 v151, v31
	v_cvt_f32_i32_e32 v150, v30
	global_store_dwordx2 v[148:149], v[164:165], off
	v_cvt_f32_i32_e32 v153, v33
	v_cvt_f32_i32_e32 v152, v32
	v_cvt_f32_i32_e32 v155, v43
	v_cvt_f32_i32_e32 v154, v42
	v_cvt_f32_i32_e32 v157, v45
	v_cvt_f32_i32_e32 v156, v44
	v_cvt_f32_i32_e32 v159, v39
	v_cvt_f32_i32_e32 v158, v38
	v_cvt_f32_i32_e32 v161, v41
	v_cvt_f32_i32_e32 v160, v40
	v_cvt_f32_i32_e32 v163, v47
	v_cvt_f32_i32_e32 v162, v46
	v_cvt_f32_i32_e32 v165, v49
	v_cvt_f32_i32_e32 v164, v48
	v_pk_mul_f32 v[152:153], v[144:145], v[152:153]
	v_pk_mul_f32 v[150:151], v[142:143], v[150:151]
	v_pk_mul_f32 v[156:157], v[136:137], v[156:157]
	v_pk_mul_f32 v[154:155], v[134:135], v[154:155]
	v_pk_mul_f32 v[160:161], v[140:141], v[160:161]
	v_pk_mul_f32 v[158:159], v[138:139], v[158:159]
	v_pk_mul_f32 v[164:165], v[132:133], v[164:165]
	v_pk_mul_f32 v[162:163], v[130:131], v[162:163]
	v_pk_mul_f32 v[160:161], v[152:153], v[160:161]
	v_pk_mul_f32 v[158:159], v[150:151], v[158:159]
	v_pk_mul_f32 v[164:165], v[156:157], v[164:165]
	v_pk_mul_f32 v[162:163], v[154:155], v[162:163]
	v_mov_b32_e32 v166, 0
	v_mov_b32_e32 v167, 0
	v_mov_b32_e32 v169, v237
	v_mul_f32_e32 v168, 0xbfb8aa3b, v169
	v_mul_f32_e32 v169, v169, v169
	v_div_scale_f32 v170, s[2:3], v169, v169, 1.0
	v_pk_mul_f32 v[150:151], v[150:151], v[168:169] op_sel_hi:[1,0]
	v_pk_mul_f32 v[152:153], v[152:153], v[168:169] op_sel_hi:[1,0]
	v_pk_mul_f32 v[154:155], v[154:155], v[168:169] op_sel_hi:[1,0]
	v_pk_mul_f32 v[156:157], v[156:157], v[168:169] op_sel_hi:[1,0]
	v_rcp_f32_e32 v168, v170
	v_div_scale_f32 v171, vcc, 1.0, v169, 1.0
	v_exp_f32_e32 v150, v150
	v_fma_f32 v172, -v170, v168, 1.0
	v_fmac_f32_e32 v168, v172, v168
	v_mul_f32_e32 v172, v171, v168
	v_fma_f32 v173, -v170, v172, v171
	v_exp_f32_e32 v151, v151
	v_exp_f32_e32 v154, v154
	v_exp_f32_e32 v155, v155
	v_fmac_f32_e32 v172, v173, v168
	v_fma_f32 v170, -v170, v172, v171
	v_div_fmas_f32 v168, v170, v168, v172
	v_div_fixup_f32 v168, v168, v169, 1.0
	v_exp_f32_e32 v152, v152
	v_exp_f32_e32 v153, v153
	v_exp_f32_e32 v156, v156
	v_exp_f32_e32 v157, v157
	v_pk_fma_f32 v[150:151], v[168:169], v[150:151], v[168:169] op_sel_hi:[0,1,0]
	v_pk_fma_f32 v[154:155], v[168:169], v[154:155], v[168:169] op_sel_hi:[0,1,0]
	v_rcp_f32_e32 v150, v150
	v_rcp_f32_e32 v151, v151
	v_rcp_f32_e32 v154, v154
	v_rcp_f32_e32 v155, v155
	v_pk_fma_f32 v[152:153], v[168:169], v[152:153], v[168:169] op_sel_hi:[0,1,0]
	v_pk_fma_f32 v[156:157], v[168:169], v[156:157], v[168:169] op_sel_hi:[0,1,0]
	v_rcp_f32_e32 v152, v152
	v_rcp_f32_e32 v153, v153
	v_rcp_f32_e32 v156, v156
	v_rcp_f32_e32 v157, v157
	v_pk_mul_f32 v[150:151], v[158:159], v[150:151]
	v_pk_mul_f32 v[154:155], v[162:163], v[154:155]
	v_med3_f32 v150, v150, s6, v208
	v_med3_f32 v151, v151, s6, v208
	v_med3_f32 v154, v154, s6, v208
	v_med3_f32 v155, v155, s6, v208
	v_cvt_pk_fp8_f32 v166, v150, v151
	v_cvt_pk_fp8_f32 v167, v154, v155
	v_pk_mul_f32 v[152:153], v[160:161], v[152:153]
	v_pk_mul_f32 v[156:157], v[164:165], v[156:157]
	v_med3_f32 v152, v152, s6, v208
	v_med3_f32 v153, v153, s6, v208
	v_med3_f32 v150, v156, s6, v208
	v_med3_f32 v151, v157, s6, v208
	v_cvt_pk_fp8_f32 v166, v152, v153 op_sel:[0,0,1]
	v_cvt_pk_fp8_f32 v167, v150, v151 op_sel:[0,0,1]
	v_cvt_f32_i32_e32 v151, v59
	v_cvt_f32_i32_e32 v150, v58
	v_cvt_f32_i32_e32 v153, v61
	global_store_dwordx2 v[148:149], v[166:167], off offset:2048
	v_cvt_f32_i32_e32 v152, v60
	v_cvt_f32_i32_e32 v155, v75
	v_cvt_f32_i32_e32 v154, v74
	v_cvt_f32_i32_e32 v157, v77
	v_cvt_f32_i32_e32 v156, v76
	v_cvt_f32_i32_e32 v159, v71
	v_cvt_f32_i32_e32 v158, v70
	v_cvt_f32_i32_e32 v161, v73
	v_cvt_f32_i32_e32 v160, v72
	v_cvt_f32_i32_e32 v163, v79
	v_cvt_f32_i32_e32 v162, v78
	v_cvt_f32_i32_e32 v165, v81
	v_cvt_f32_i32_e32 v164, v80
	v_pk_mul_f32 v[152:153], v[144:145], v[152:153]
	v_pk_mul_f32 v[150:151], v[142:143], v[150:151]
	v_pk_mul_f32 v[156:157], v[136:137], v[156:157]
	v_pk_mul_f32 v[154:155], v[134:135], v[154:155]
	v_pk_mul_f32 v[160:161], v[140:141], v[160:161]
	v_pk_mul_f32 v[158:159], v[138:139], v[158:159]
	v_pk_mul_f32 v[164:165], v[132:133], v[164:165]
	v_pk_mul_f32 v[162:163], v[130:131], v[162:163]
	v_pk_mul_f32 v[160:161], v[152:153], v[160:161]
	v_pk_mul_f32 v[158:159], v[150:151], v[158:159]
	v_pk_mul_f32 v[164:165], v[156:157], v[164:165]
	v_pk_mul_f32 v[162:163], v[154:155], v[162:163]
	v_mov_b32_e32 v166, 0
	v_mov_b32_e32 v167, 0
	v_mov_b32_e32 v169, v238
	v_mul_f32_e32 v168, 0xbfb8aa3b, v169
	v_mul_f32_e32 v169, v169, v169
	v_div_scale_f32 v170, s[2:3], v169, v169, 1.0
	v_pk_mul_f32 v[150:151], v[150:151], v[168:169] op_sel_hi:[1,0]
	v_pk_mul_f32 v[152:153], v[152:153], v[168:169] op_sel_hi:[1,0]
	v_pk_mul_f32 v[154:155], v[154:155], v[168:169] op_sel_hi:[1,0]
	v_pk_mul_f32 v[156:157], v[156:157], v[168:169] op_sel_hi:[1,0]
	v_rcp_f32_e32 v168, v170
	v_div_scale_f32 v171, vcc, 1.0, v169, 1.0
	v_exp_f32_e32 v150, v150
	v_fma_f32 v172, -v170, v168, 1.0
	v_fmac_f32_e32 v168, v172, v168
	v_mul_f32_e32 v172, v171, v168
	v_fma_f32 v173, -v170, v172, v171
	v_exp_f32_e32 v151, v151
	v_exp_f32_e32 v154, v154
	v_exp_f32_e32 v155, v155
	v_fmac_f32_e32 v172, v173, v168
	v_fma_f32 v170, -v170, v172, v171
	v_div_fmas_f32 v168, v170, v168, v172
	v_div_fixup_f32 v168, v168, v169, 1.0
	v_exp_f32_e32 v152, v152
	v_exp_f32_e32 v153, v153
	v_exp_f32_e32 v156, v156
	v_exp_f32_e32 v157, v157
	v_pk_fma_f32 v[150:151], v[168:169], v[150:151], v[168:169] op_sel_hi:[0,1,0]
	v_pk_fma_f32 v[154:155], v[168:169], v[154:155], v[168:169] op_sel_hi:[0,1,0]
	v_rcp_f32_e32 v150, v150
	v_rcp_f32_e32 v151, v151
	v_rcp_f32_e32 v154, v154
	v_rcp_f32_e32 v155, v155
	v_pk_fma_f32 v[152:153], v[168:169], v[152:153], v[168:169] op_sel_hi:[0,1,0]
	v_pk_fma_f32 v[156:157], v[168:169], v[156:157], v[168:169] op_sel_hi:[0,1,0]
	v_rcp_f32_e32 v152, v152
	v_rcp_f32_e32 v153, v153
	v_rcp_f32_e32 v156, v156
	v_rcp_f32_e32 v157, v157
	v_pk_mul_f32 v[150:151], v[158:159], v[150:151]
	v_pk_mul_f32 v[154:155], v[162:163], v[154:155]
	v_med3_f32 v150, v150, s6, v208
	v_med3_f32 v151, v151, s6, v208
	v_med3_f32 v154, v154, s6, v208
	v_med3_f32 v155, v155, s6, v208
	v_cvt_pk_fp8_f32 v166, v150, v151
	v_cvt_pk_fp8_f32 v167, v154, v155
	v_pk_mul_f32 v[152:153], v[160:161], v[152:153]
	v_pk_mul_f32 v[156:157], v[164:165], v[156:157]
	v_med3_f32 v152, v152, s6, v208
	v_med3_f32 v153, v153, s6, v208
	v_med3_f32 v150, v156, s6, v208
	v_med3_f32 v151, v157, s6, v208
	v_cvt_pk_fp8_f32 v166, v152, v153 op_sel:[0,0,1]
	v_cvt_pk_fp8_f32 v167, v150, v151 op_sel:[0,0,1]
	v_add_co_u32_e32 v148, vcc, s71, v148
	v_cvt_f32_i32_e32 v151, v93
	s_nop 0
	v_addc_co_u32_e32 v149, vcc, 0, v149, vcc
	global_store_dwordx2 v[148:149], v[166:167], off
	v_cvt_f32_i32_e32 v147, v91
	v_cvt_f32_i32_e32 v146, v90
	v_cvt_f32_i32_e32 v150, v92
	v_cvt_f32_i32_e32 v153, v107
	v_cvt_f32_i32_e32 v152, v106
	v_cvt_f32_i32_e32 v155, v109
	v_cvt_f32_i32_e32 v154, v108
	v_cvt_f32_i32_e32 v157, v103
	v_cvt_f32_i32_e32 v156, v102
	v_cvt_f32_i32_e32 v159, v105
	v_cvt_f32_i32_e32 v158, v104
	v_cvt_f32_i32_e32 v161, v111
	v_cvt_f32_i32_e32 v160, v110
	v_cvt_f32_i32_e32 v163, v113
	v_cvt_f32_i32_e32 v162, v112
	v_pk_mul_f32 v[142:143], v[142:143], v[146:147]
	v_pk_mul_f32 v[144:145], v[144:145], v[150:151]
	v_pk_mul_f32 v[136:137], v[136:137], v[154:155]
	v_pk_mul_f32 v[134:135], v[134:135], v[152:153]
	v_pk_mul_f32 v[140:141], v[140:141], v[158:159]
	v_pk_mul_f32 v[138:139], v[138:139], v[156:157]
	v_pk_mul_f32 v[132:133], v[132:133], v[162:163]
	v_pk_mul_f32 v[130:131], v[130:131], v[160:161]
	v_pk_mul_f32 v[140:141], v[144:145], v[140:141]
	v_pk_mul_f32 v[138:139], v[142:143], v[138:139]
	v_pk_mul_f32 v[132:133], v[136:137], v[132:133]
	v_pk_mul_f32 v[130:131], v[134:135], v[130:131]
	v_mov_b32_e32 v164, 0
	v_mov_b32_e32 v165, 0
	v_mov_b32_e32 v166, v239
	v_mul_f32_e32 v147, v166, v166
	v_mul_f32_e32 v146, 0xbfb8aa3b, v166
	v_div_scale_f32 v150, s[2:3], v147, v147, 1.0
	v_pk_mul_f32 v[142:143], v[142:143], v[146:147] op_sel_hi:[1,0]
	v_pk_mul_f32 v[144:145], v[144:145], v[146:147] op_sel_hi:[1,0]
	v_pk_mul_f32 v[134:135], v[134:135], v[146:147] op_sel_hi:[1,0]
	v_pk_mul_f32 v[136:137], v[136:137], v[146:147] op_sel_hi:[1,0]
	v_rcp_f32_e32 v146, v150
	v_div_scale_f32 v151, vcc, 1.0, v147, 1.0
	v_exp_f32_e32 v142, v142
	v_fma_f32 v152, -v150, v146, 1.0
	v_fmac_f32_e32 v146, v152, v146
	v_mul_f32_e32 v152, v151, v146
	v_fma_f32 v153, -v150, v152, v151
	v_exp_f32_e32 v143, v143
	v_exp_f32_e32 v134, v134
	v_exp_f32_e32 v135, v135
	v_fmac_f32_e32 v152, v153, v146
	v_fma_f32 v150, -v150, v152, v151
	v_div_fmas_f32 v146, v150, v146, v152
	v_div_fixup_f32 v146, v146, v147, 1.0
	v_exp_f32_e32 v144, v144
	v_exp_f32_e32 v145, v145
	v_exp_f32_e32 v136, v136
	v_exp_f32_e32 v137, v137
	v_pk_fma_f32 v[142:143], v[146:147], v[142:143], v[146:147] op_sel_hi:[0,1,0]
	v_pk_fma_f32 v[134:135], v[146:147], v[134:135], v[146:147] op_sel_hi:[0,1,0]
	v_rcp_f32_e32 v142, v142
	v_rcp_f32_e32 v143, v143
	v_rcp_f32_e32 v134, v134
	v_rcp_f32_e32 v135, v135
	v_pk_fma_f32 v[144:145], v[146:147], v[144:145], v[146:147] op_sel_hi:[0,1,0]
	v_pk_fma_f32 v[136:137], v[146:147], v[136:137], v[146:147] op_sel_hi:[0,1,0]
	v_rcp_f32_e32 v144, v144
	v_rcp_f32_e32 v145, v145
	v_rcp_f32_e32 v136, v136
	v_rcp_f32_e32 v137, v137
	v_pk_mul_f32 v[138:139], v[138:139], v[142:143]
	v_pk_mul_f32 v[130:131], v[130:131], v[134:135]
	v_med3_f32 v134, v138, s6, v208
	v_med3_f32 v135, v139, s6, v208
	v_med3_f32 v130, v130, s6, v208
	v_med3_f32 v131, v131, s6, v208
	v_cvt_pk_fp8_f32 v164, v134, v135
	v_cvt_pk_fp8_f32 v165, v130, v131
	v_pk_mul_f32 v[140:141], v[140:141], v[144:145]
	v_pk_mul_f32 v[132:133], v[132:133], v[136:137]
	v_med3_f32 v136, v140, s6, v208
	v_med3_f32 v137, v141, s6, v208
	v_med3_f32 v130, v132, s6, v208
	v_med3_f32 v131, v133, s6, v208
	v_cvt_pk_fp8_f32 v164, v136, v137 op_sel:[0,0,1]
	v_cvt_pk_fp8_f32 v165, v130, v131 op_sel:[0,0,1]
	s_andn2_b64 vcc, exec, s[28:29]
	s_mov_b64 s[2:3], -1
	global_store_dwordx2 v[148:149], v[164:165], off offset:2048
	s_cbranch_vccnz .LBB0_845
	s_andn2_b64 vcc, exec, s[4:5]
	s_cbranch_vccnz .LBB0_844
	s_barrier
	s_branch .LBB0_844

.LBB0_1084:
	v_add_u32_e32 v130, 0, v202
	v_add_u32_e32 v131, 0x10000, v130
	v_add_u32_e32 v130, 0x14000, v130
	ds_read_b128 v[158:161], v131
	ds_read_b128 v[154:157], v131 offset:1024
	ds_read_b128 v[150:153], v131 offset:2048
	ds_read_b128 v[142:145], v131 offset:3072
	ds_read_b128 v[146:149], v130
	ds_read_b128 v[138:141], v130 offset:1024
	ds_read_b128 v[134:137], v130 offset:2048
	ds_read_b128 v[130:133], v130 offset:3072
	s_add_u32 s43, s28, s48
	s_addc_u32 s80, s29, s49
	s_add_u32 s14, s43, 0x80
	s_addc_u32 s15, s80, 0
	v_mov_b32_e32 v205, v196
	ds_read_b128 v[190:193], v204
	ds_read_b128 v[186:189], v204 offset:1024
	ds_read_b128 v[182:185], v204 offset:2048
	ds_read_b128 v[178:181], v204 offset:3072
	ds_read_b128 v[174:177], v204 offset:4096
	ds_read_b128 v[170:173], v204 offset:5120
	ds_read_b128 v[166:169], v204 offset:6144
	ds_read_b128 v[162:165], v204 offset:7168
	s_add_i32 m0, s5, 0x8000
	s_nop 0
	global_load_lds_dwordx4 v205, s[14:15]
	v_mov_b32_e32 v205, v198
	s_add_i32 m0, s5, 0xa000
	s_nop 0
	global_load_lds_dwordx4 v205, s[14:15]
	s_add_u32 s14, s43, 0x40080
	s_addc_u32 s15, s80, 0
	v_mov_b32_e32 v205, v196
	s_add_i32 m0, s5, 0xc000
	s_nop 0
	global_load_lds_dwordx4 v205, s[14:15]
	v_mov_b32_e32 v205, v198
	s_add_i32 m0, s5, 0xe000
	s_cmp_lg_u32 s41, -2
	global_load_lds_dwordx4 v205, s[14:15]
	v_lshl_or_b32 v242, s79, 8, v203
	v_lshl_add_u32 v240, s76, 8, v201
	v_ashrrev_i32_e32 v243, 31, v242
	v_ashrrev_i32_e32 v241, 31, v240
	v_lshl_add_u64 v[242:243], v[242:243], 2, s[8:9]
	v_lshl_add_u64 v[240:241], v[240:241], 2, s[38:39]
	global_load_dwordx4 v[210:213], v[242:243], off
	global_load_dwordx4 v[214:217], v[242:243], off offset:16
	global_load_dwordx4 v[218:221], v[242:243], off offset:512
	global_load_dwordx4 v[222:225], v[242:243], off offset:528
	global_load_dword v232, v[240:241], off
	global_load_dword v233, v[240:241], off offset:64
	global_load_dword v234, v[240:241], off offset:128
	global_load_dword v235, v[240:241], off offset:192
	global_load_dword v236, v[240:241], off offset:512
	global_load_dword v237, v[240:241], off offset:576
	global_load_dword v238, v[240:241], off offset:640
	global_load_dword v239, v[240:241], off offset:704
	s_cselect_b64 s[64:65], -1, 0
	s_and_b64 vcc, exec, s[64:65]
	s_cbranch_vccnz .LBB0_1087
	s_mov_b64 s[0:1], 0
	s_andn2_b64 vcc, exec, s[2:3]
	s_mov_b64 s[14:15], s[30:31]
	s_mov_b64 s[26:27], s[28:29]
	s_cbranch_vccnz .LBB0_1088
	s_mov_b64 s[0:1], -1
	s_mov_b64 s[14:15], s[46:47]
	s_mov_b64 s[26:27], s[44:45]
	s_mov_b32 s4, s42
	s_mov_b32 s72, s40
	s_branch .LBB0_1088

.LBB0_1088:
	s_waitcnt vmcnt(20)
	s_waitcnt lgkmcnt(0)
	s_barrier
	s_setprio 1
	v_mfma_i32_16x16x64_i8 v[18:21], v[158:161], v[190:193], 0
	s_nop 0
	v_mfma_i32_16x16x64_i8 v[18:21], v[154:157], v[186:189], v[18:21]
	v_mfma_i32_16x16x64_i8 v[22:25], v[150:153], v[190:193], 0
	s_nop 0
	v_mfma_i32_16x16x64_i8 v[22:25], v[142:145], v[186:189], v[22:25]
	v_mfma_i32_16x16x64_i8 v[26:29], v[146:149], v[190:193], 0
	s_nop 0
	v_mfma_i32_16x16x64_i8 v[26:29], v[138:141], v[186:189], v[26:29]
	v_mfma_i32_16x16x64_i8 v[34:37], v[134:137], v[190:193], 0
	s_nop 0
	v_mfma_i32_16x16x64_i8 v[34:37], v[130:133], v[186:189], v[34:37]
	v_mfma_i32_16x16x64_i8 v[50:53], v[158:161], v[182:185], 0
	s_nop 0
	v_mfma_i32_16x16x64_i8 v[50:53], v[154:157], v[178:181], v[50:53]
	v_mfma_i32_16x16x64_i8 v[62:65], v[150:153], v[182:185], 0
	s_nop 0
	v_mfma_i32_16x16x64_i8 v[62:65], v[142:145], v[178:181], v[62:65]
	v_mfma_i32_16x16x64_i8 v[54:57], v[146:149], v[182:185], 0
	s_nop 0
	v_mfma_i32_16x16x64_i8 v[54:57], v[138:141], v[178:181], v[54:57]
	v_mfma_i32_16x16x64_i8 v[66:69], v[134:137], v[182:185], 0
	s_nop 0
	v_mfma_i32_16x16x64_i8 v[66:69], v[130:133], v[178:181], v[66:69]
	v_mfma_i32_16x16x64_i8 v[82:85], v[158:161], v[174:177], 0
	s_nop 0
	v_mfma_i32_16x16x64_i8 v[82:85], v[154:157], v[170:173], v[82:85]
	v_mfma_i32_16x16x64_i8 v[94:97], v[150:153], v[174:177], 0
	s_nop 0
	v_mfma_i32_16x16x64_i8 v[94:97], v[142:145], v[170:173], v[94:97]
	v_mfma_i32_16x16x64_i8 v[86:89], v[146:149], v[174:177], 0
	s_nop 0
	v_mfma_i32_16x16x64_i8 v[86:89], v[138:141], v[170:173], v[86:89]
	v_mfma_i32_16x16x64_i8 v[98:101], v[134:137], v[174:177], 0
	s_nop 0
	v_mfma_i32_16x16x64_i8 v[98:101], v[130:133], v[170:173], v[98:101]
	v_mfma_i32_16x16x64_i8 v[114:117], v[158:161], v[166:169], 0
	s_nop 0
	v_mfma_i32_16x16x64_i8 v[114:117], v[154:157], v[162:165], v[114:117]
	v_mfma_i32_16x16x64_i8 v[122:125], v[150:153], v[166:169], 0
	s_nop 0
	v_mfma_i32_16x16x64_i8 v[122:125], v[142:145], v[162:165], v[122:125]
	v_mfma_i32_16x16x64_i8 v[118:121], v[146:149], v[166:169], 0
	s_nop 0
	v_mfma_i32_16x16x64_i8 v[118:121], v[138:141], v[162:165], v[118:121]
	v_mfma_i32_16x16x64_i8 v[126:129], v[134:137], v[166:169], 0
	s_nop 0
	v_mfma_i32_16x16x64_i8 v[126:129], v[130:133], v[162:165], v[126:129]
	s_setprio 0
	s_barrier
	s_add_u32 s81, s77, s48
	s_addc_u32 s82, s78, s49
	s_cmp_eq_u32 s41, 12
	s_cselect_b64 s[66:67], -1, 0
	s_and_b64 s[74:75], s[66:67], exec
	s_cselect_b32 s53, s53, s82
	s_cselect_b32 s52, s52, s81
	s_mov_b64 s[74:75], s[52:53]
	v_mov_b32_e32 v205, v197
	s_mov_b32 m0, s33
	s_waitcnt lgkmcnt(0)
	ds_read_b128 v[190:193], v204 offset:16384
	ds_read_b128 v[186:189], v204 offset:17408
	ds_read_b128 v[182:185], v204 offset:18432
	ds_read_b128 v[178:181], v204 offset:19456
	ds_read_b128 v[174:177], v204 offset:20480
	ds_read_b128 v[170:173], v204 offset:21504
	ds_read_b128 v[166:169], v204 offset:22528
	ds_read_b128 v[162:165], v204 offset:23552
	s_nop 0
	global_load_lds_dwordx4 v205, s[74:75]
	v_mov_b32_e32 v205, v199
	s_mov_b32 m0, s35
	s_nop 0
	global_load_lds_dwordx4 v205, s[74:75]
	s_add_u32 s74, s52, 0x40000
	s_addc_u32 s75, s53, 0
	v_mov_b32_e32 v205, v197
	s_mov_b32 m0, s60
	s_nop 0
	global_load_lds_dwordx4 v205, s[74:75]
	v_mov_b32_e32 v205, v199
	s_mov_b32 m0, s61
	s_nop 0
	global_load_lds_dwordx4 v205, s[74:75]
	s_waitcnt vmcnt(18)
	s_waitcnt lgkmcnt(0)
	s_barrier
	s_setprio 1
	v_mfma_i32_16x16x64_i8 v[2:5], v[158:161], v[190:193], 0
	s_nop 0
	v_mfma_i32_16x16x64_i8 v[2:5], v[154:157], v[186:189], v[2:5]
	v_mfma_i32_16x16x64_i8 v[6:9], v[150:153], v[190:193], 0
	s_nop 0
	v_mfma_i32_16x16x64_i8 v[6:9], v[142:145], v[186:189], v[6:9]
	v_mfma_i32_16x16x64_i8 v[10:13], v[146:149], v[190:193], 0
	s_nop 0
	v_mfma_i32_16x16x64_i8 v[10:13], v[138:141], v[186:189], v[10:13]
	v_mfma_i32_16x16x64_i8 v[14:17], v[134:137], v[190:193], 0
	s_nop 0
	v_mfma_i32_16x16x64_i8 v[14:17], v[130:133], v[186:189], v[14:17]
	v_mfma_i32_16x16x64_i8 v[30:33], v[158:161], v[182:185], 0
	s_nop 0
	v_mfma_i32_16x16x64_i8 v[30:33], v[154:157], v[178:181], v[30:33]
	v_mfma_i32_16x16x64_i8 v[42:45], v[150:153], v[182:185], 0
	s_nop 0
	v_mfma_i32_16x16x64_i8 v[42:45], v[142:145], v[178:181], v[42:45]
	v_mfma_i32_16x16x64_i8 v[38:41], v[146:149], v[182:185], 0
	s_nop 0
	v_mfma_i32_16x16x64_i8 v[38:41], v[138:141], v[178:181], v[38:41]
	v_mfma_i32_16x16x64_i8 v[46:49], v[134:137], v[182:185], 0
	s_nop 0
	v_mfma_i32_16x16x64_i8 v[46:49], v[130:133], v[178:181], v[46:49]
	v_mfma_i32_16x16x64_i8 v[58:61], v[158:161], v[174:177], 0
	s_nop 0
	v_mfma_i32_16x16x64_i8 v[58:61], v[154:157], v[170:173], v[58:61]
	v_mfma_i32_16x16x64_i8 v[74:77], v[150:153], v[174:177], 0
	s_nop 0
	v_mfma_i32_16x16x64_i8 v[74:77], v[142:145], v[170:173], v[74:77]
	v_mfma_i32_16x16x64_i8 v[70:73], v[146:149], v[174:177], 0
	s_nop 0
	v_mfma_i32_16x16x64_i8 v[70:73], v[138:141], v[170:173], v[70:73]
	v_mfma_i32_16x16x64_i8 v[78:81], v[134:137], v[174:177], 0
	s_nop 0
	v_mfma_i32_16x16x64_i8 v[78:81], v[130:133], v[170:173], v[78:81]
	v_mfma_i32_16x16x64_i8 v[90:93], v[158:161], v[166:169], 0
	s_nop 0
	v_mfma_i32_16x16x64_i8 v[90:93], v[154:157], v[162:165], v[90:93]
	v_mfma_i32_16x16x64_i8 v[106:109], v[150:153], v[166:169], 0
	s_nop 0
	v_mfma_i32_16x16x64_i8 v[106:109], v[142:145], v[162:165], v[106:109]
	v_mfma_i32_16x16x64_i8 v[102:105], v[146:149], v[166:169], 0
	s_nop 0
	v_mfma_i32_16x16x64_i8 v[102:105], v[138:141], v[162:165], v[102:105]
	v_mfma_i32_16x16x64_i8 v[110:113], v[134:137], v[166:169], 0
	s_nop 0
	v_mfma_i32_16x16x64_i8 v[110:113], v[130:133], v[162:165], v[110:113]
	s_setprio 0
	s_barrier
	s_add_u32 s43, s43, 0x100
	s_addc_u32 s74, s80, 0
	s_and_b64 s[64:65], s[66:67], exec
	s_cselect_b32 s65, s51, s74
	s_cselect_b32 s64, s50, s43
	s_add_u32 s50, s52, 0x80
	s_addc_u32 s51, s53, 0
	s_add_i32 s43, 0, 0x18000
	s_add_i32 s74, 0, 0x1c000
	v_add_u32_e32 v130, s43, v202
	v_add_u32_e32 v131, s74, v202
	ds_read_b128 v[158:161], v130
	ds_read_b128 v[154:157], v130 offset:1024
	ds_read_b128 v[150:153], v130 offset:2048
	ds_read_b128 v[146:149], v130 offset:3072
	ds_read_b128 v[142:145], v131
	ds_read_b128 v[138:141], v131 offset:1024
	ds_read_b128 v[134:137], v131 offset:2048
	ds_read_b128 v[130:133], v131 offset:3072
	s_mov_b64 s[66:67], s[64:65]
	v_mov_b32_e32 v205, v196
	s_mov_b32 m0, s5
	s_waitcnt lgkmcnt(0)
	ds_read_b128 v[162:165], v204 offset:32768
	ds_read_b128 v[166:169], v204 offset:33792
	ds_read_b128 v[170:173], v204 offset:34816
	ds_read_b128 v[174:177], v204 offset:35840
	ds_read_b128 v[178:181], v204 offset:36864
	ds_read_b128 v[182:185], v204 offset:37888
	ds_read_b128 v[186:189], v204 offset:38912
	ds_read_b128 v[190:193], v204 offset:39936
	s_add_u32 s64, s64, 0x40000
	global_load_lds_dwordx4 v205, s[66:67]
	v_mov_b32_e32 v205, v198
	s_mov_b32 m0, s62
	s_addc_u32 s65, s65, 0
	global_load_lds_dwordx4 v205, s[66:67]
	v_mov_b32_e32 v205, v196
	s_mov_b32 m0, s63
	s_nop 0
	global_load_lds_dwordx4 v205, s[64:65]
	v_mov_b32_e32 v205, v198
	s_mov_b32 m0, s69
	s_nop 0
	global_load_lds_dwordx4 v205, s[64:65]
	s_waitcnt vmcnt(8)
	s_waitcnt lgkmcnt(0)
	s_barrier
	s_setprio 1
	s_waitcnt lgkmcnt(0)
	v_mfma_i32_16x16x64_i8 v[18:21], v[158:161], v[162:165], v[18:21]
	s_nop 0
	v_mfma_i32_16x16x64_i8 v[18:21], v[154:157], v[166:169], v[18:21]
	v_mfma_i32_16x16x64_i8 v[22:25], v[150:153], v[162:165], v[22:25]
	s_nop 0
	v_mfma_i32_16x16x64_i8 v[22:25], v[146:149], v[166:169], v[22:25]
	v_mfma_i32_16x16x64_i8 v[26:29], v[142:145], v[162:165], v[26:29]
	s_nop 0
	v_mfma_i32_16x16x64_i8 v[26:29], v[138:141], v[166:169], v[26:29]
	v_mfma_i32_16x16x64_i8 v[34:37], v[134:137], v[162:165], v[34:37]
	s_nop 0
	v_mfma_i32_16x16x64_i8 v[34:37], v[130:133], v[166:169], v[34:37]
	v_mfma_i32_16x16x64_i8 v[50:53], v[158:161], v[170:173], v[50:53]
	s_nop 0
	v_mfma_i32_16x16x64_i8 v[50:53], v[154:157], v[174:177], v[50:53]
	v_mfma_i32_16x16x64_i8 v[62:65], v[150:153], v[170:173], v[62:65]
	s_nop 0
	v_mfma_i32_16x16x64_i8 v[62:65], v[146:149], v[174:177], v[62:65]
	v_mfma_i32_16x16x64_i8 v[54:57], v[142:145], v[170:173], v[54:57]
	s_nop 0
	v_mfma_i32_16x16x64_i8 v[54:57], v[138:141], v[174:177], v[54:57]
	v_mfma_i32_16x16x64_i8 v[66:69], v[134:137], v[170:173], v[66:69]
	s_nop 0
	v_mfma_i32_16x16x64_i8 v[66:69], v[130:133], v[174:177], v[66:69]
	v_mfma_i32_16x16x64_i8 v[82:85], v[158:161], v[178:181], v[82:85]
	s_nop 0
	v_mfma_i32_16x16x64_i8 v[82:85], v[154:157], v[182:185], v[82:85]
	v_mfma_i32_16x16x64_i8 v[94:97], v[150:153], v[178:181], v[94:97]
	s_nop 0
	v_mfma_i32_16x16x64_i8 v[94:97], v[146:149], v[182:185], v[94:97]
	v_mfma_i32_16x16x64_i8 v[86:89], v[142:145], v[178:181], v[86:89]
	s_nop 0
	v_mfma_i32_16x16x64_i8 v[86:89], v[138:141], v[182:185], v[86:89]
	v_mfma_i32_16x16x64_i8 v[98:101], v[134:137], v[178:181], v[98:101]
	s_nop 0
	v_mfma_i32_16x16x64_i8 v[98:101], v[130:133], v[182:185], v[98:101]
	v_mfma_i32_16x16x64_i8 v[114:117], v[158:161], v[186:189], v[114:117]
	s_nop 0
	v_mfma_i32_16x16x64_i8 v[114:117], v[154:157], v[190:193], v[114:117]
	v_mfma_i32_16x16x64_i8 v[122:125], v[150:153], v[186:189], v[122:125]
	s_nop 0
	v_mfma_i32_16x16x64_i8 v[122:125], v[146:149], v[190:193], v[122:125]
	v_mfma_i32_16x16x64_i8 v[118:121], v[142:145], v[186:189], v[118:121]
	s_nop 0
	v_mfma_i32_16x16x64_i8 v[118:121], v[138:141], v[190:193], v[118:121]
	v_mfma_i32_16x16x64_i8 v[126:129], v[134:137], v[186:189], v[126:129]
	s_nop 0
	v_mfma_i32_16x16x64_i8 v[126:129], v[130:133], v[190:193], v[126:129]
	s_setprio 0
	s_barrier
	v_mov_b32_e32 v205, v197
	s_add_i32 s43, s43, s10
	ds_read_b128 v[162:165], v204 offset:49152
	ds_read_b128 v[166:169], v204 offset:50176
	ds_read_b128 v[170:173], v204 offset:51200
	ds_read_b128 v[174:177], v204 offset:52224
	ds_read_b128 v[178:181], v204 offset:53248
	ds_read_b128 v[182:185], v204 offset:54272
	ds_read_b128 v[186:189], v204 offset:55296
	ds_read_b128 v[190:193], v204 offset:56320
	s_mov_b32 m0, s43
	s_nop 0
	global_load_lds_dwordx4 v205, s[50:51]
	v_mov_b32_e32 v205, v199
	s_add_i32 m0, s43, 0x2000
	s_nop 0
	global_load_lds_dwordx4 v205, s[50:51]
	s_add_u32 s50, s52, 0x40080
	s_addc_u32 s51, s53, 0
	v_mov_b32_e32 v205, v197
	s_add_i32 s43, s74, s10
	s_mov_b32 m0, s43
	s_nop 0
	global_load_lds_dwordx4 v205, s[50:51]
	v_mov_b32_e32 v205, v199
	s_add_i32 m0, s43, 0x2000
	s_nop 0
	global_load_lds_dwordx4 v205, s[50:51]
	s_waitcnt vmcnt(6)
	s_waitcnt lgkmcnt(0)
	s_barrier
	s_setprio 1
	s_waitcnt lgkmcnt(0)
	v_mfma_i32_16x16x64_i8 v[2:5], v[158:161], v[162:165], v[2:5]
	s_nop 0
	v_mfma_i32_16x16x64_i8 v[2:5], v[154:157], v[166:169], v[2:5]
	v_mfma_i32_16x16x64_i8 v[6:9], v[150:153], v[162:165], v[6:9]
	s_nop 0
	v_mfma_i32_16x16x64_i8 v[6:9], v[146:149], v[166:169], v[6:9]
	v_mfma_i32_16x16x64_i8 v[10:13], v[142:145], v[162:165], v[10:13]
	s_nop 0
	v_mfma_i32_16x16x64_i8 v[10:13], v[138:141], v[166:169], v[10:13]
	v_mfma_i32_16x16x64_i8 v[14:17], v[134:137], v[162:165], v[14:17]
	s_nop 0
	v_mfma_i32_16x16x64_i8 v[14:17], v[130:133], v[166:169], v[14:17]
	v_mfma_i32_16x16x64_i8 v[30:33], v[158:161], v[170:173], v[30:33]
	s_nop 0
	v_mfma_i32_16x16x64_i8 v[30:33], v[154:157], v[174:177], v[30:33]
	v_mfma_i32_16x16x64_i8 v[42:45], v[150:153], v[170:173], v[42:45]
	s_nop 0
	v_mfma_i32_16x16x64_i8 v[42:45], v[146:149], v[174:177], v[42:45]
	v_mfma_i32_16x16x64_i8 v[38:41], v[142:145], v[170:173], v[38:41]
	s_nop 0
	v_mfma_i32_16x16x64_i8 v[38:41], v[138:141], v[174:177], v[38:41]
	v_mfma_i32_16x16x64_i8 v[46:49], v[134:137], v[170:173], v[46:49]
	s_nop 0
	v_mfma_i32_16x16x64_i8 v[46:49], v[130:133], v[174:177], v[46:49]
	v_mfma_i32_16x16x64_i8 v[58:61], v[158:161], v[178:181], v[58:61]
	s_nop 0
	v_mfma_i32_16x16x64_i8 v[58:61], v[154:157], v[182:185], v[58:61]
	v_mfma_i32_16x16x64_i8 v[74:77], v[150:153], v[178:181], v[74:77]
	s_nop 0
	v_mfma_i32_16x16x64_i8 v[74:77], v[146:149], v[182:185], v[74:77]
	v_mfma_i32_16x16x64_i8 v[70:73], v[142:145], v[178:181], v[70:73]
	s_nop 0
	v_mfma_i32_16x16x64_i8 v[70:73], v[138:141], v[182:185], v[70:73]
	v_mfma_i32_16x16x64_i8 v[78:81], v[134:137], v[178:181], v[78:81]
	s_nop 0
	v_mfma_i32_16x16x64_i8 v[78:81], v[130:133], v[182:185], v[78:81]
	v_mfma_i32_16x16x64_i8 v[90:93], v[158:161], v[186:189], v[90:93]
	s_nop 0
	v_mfma_i32_16x16x64_i8 v[90:93], v[154:157], v[190:193], v[90:93]
	v_mfma_i32_16x16x64_i8 v[106:109], v[150:153], v[186:189], v[106:109]
	s_nop 0
	v_mfma_i32_16x16x64_i8 v[106:109], v[146:149], v[190:193], v[106:109]
	v_mfma_i32_16x16x64_i8 v[102:105], v[142:145], v[186:189], v[102:105]
	s_nop 0
	v_mfma_i32_16x16x64_i8 v[102:105], v[138:141], v[190:193], v[102:105]
	v_mfma_i32_16x16x64_i8 v[110:113], v[134:137], v[186:189], v[110:113]
	s_nop 0
	v_mfma_i32_16x16x64_i8 v[110:113], v[130:133], v[190:193], v[110:113]
	s_setprio 0
	s_barrier
	s_add_i32 s41, s41, 2
	s_add_u32 s48, s48, 0x100
	s_addc_u32 s49, s49, 0
	s_cmp_gt_u32 s41, 13
	s_cbranch_scc1 .LBB0_1098
	s_mov_b64 s[52:53], s[14:15]
	s_mov_b64 s[50:51], s[26:27]

.LBB0_1100:
	v_lshl_or_b32 v148, s79, 8, v203
	v_lshl_add_u32 v150, s76, 8, v201
	v_ashrrev_i32_e32 v149, 31, v148
	v_ashrrev_i32_e32 v151, 31, v150
	s_nop 15
	s_nop 7
	v_lshl_add_u64 v[130:131], v[148:149], 2, s[8:9]
	v_lshl_add_u64 v[146:147], v[150:151], 2, s[38:39]
	v_mov_b32_e32 v154, v232
	v_mov_b32_e32 v142, v210
	v_mov_b32_e32 v143, v211
	v_mov_b32_e32 v144, v212
	v_mov_b32_e32 v145, v213
	v_mov_b32_e32 v138, v214
	v_mov_b32_e32 v139, v215
	v_mov_b32_e32 v140, v216
	v_mov_b32_e32 v141, v217
	v_mov_b32_e32 v134, v218
	v_mov_b32_e32 v135, v219
	v_mov_b32_e32 v136, v220
	v_mov_b32_e32 v137, v221
	s_nop 0
	v_mov_b32_e32 v130, v222
	v_mov_b32_e32 v131, v223
	v_mov_b32_e32 v132, v224
	v_mov_b32_e32 v133, v225
	v_cvt_f32_i32_e32 v157, v19
	v_cvt_f32_i32_e32 v156, v18
	v_cvt_f32_i32_e32 v159, v21
	v_cvt_f32_i32_e32 v158, v20
	v_cvt_f32_i32_e32 v161, v23
	v_cvt_f32_i32_e32 v160, v22
	v_cvt_f32_i32_e32 v163, v25
	v_cvt_f32_i32_e32 v162, v24
	v_cvt_f32_i32_e32 v165, v27
	v_cvt_f32_i32_e32 v164, v26
	v_cvt_f32_i32_e32 v167, v29
	v_cvt_f32_i32_e32 v166, v28
	v_cvt_f32_i32_e32 v169, v35
	v_cvt_f32_i32_e32 v168, v34
	v_cvt_f32_i32_e32 v171, v37
	v_cvt_f32_i32_e32 v170, v36
	v_lshlrev_b64 v[174:175], 12, v[150:151]
	v_or_b32_e32 v172, 16, v150
	v_lshlrev_b64 v[152:153], 1, v[148:149]
	v_lshl_add_u64 v[148:149], s[36:37], 0, v[174:175]
	v_ashrrev_i32_e32 v173, 31, v172
	v_lshl_add_u64 v[148:149], v[148:149], 0, v[152:153]
	v_lshl_add_u64 v[174:175], v[172:173], 2, s[38:39]
	v_lshlrev_b64 v[172:173], 12, v[172:173]
	v_lshl_add_u64 v[172:173], s[36:37], 0, v[172:173]
	v_lshl_add_u64 v[172:173], v[172:173], 0, v[152:153]
	s_mov_b32 s28, 0x80000
	s_mov_b64 s[2:3], 0x80000
	v_pk_mul_f32 v[176:177], v[142:143], v[154:155] op_sel_hi:[1,0]
	v_pk_mul_f32 v[178:179], v[144:145], v[154:155] op_sel_hi:[1,0]
	v_pk_mul_f32 v[180:181], v[138:139], v[154:155] op_sel_hi:[1,0]
	v_pk_mul_f32 v[182:183], v[140:141], v[154:155] op_sel_hi:[1,0]
	v_pk_mul_f32 v[184:185], v[134:135], v[154:155] op_sel_hi:[1,0]
	v_pk_mul_f32 v[186:187], v[136:137], v[154:155] op_sel_hi:[1,0]
	v_pk_mul_f32 v[188:189], v[130:131], v[154:155] op_sel_hi:[1,0]
	v_pk_mul_f32 v[154:155], v[132:133], v[154:155] op_sel_hi:[1,0]
	v_pk_mul_f32 v[158:159], v[178:179], v[158:159]
	v_pk_mul_f32 v[156:157], v[176:177], v[156:157]
	v_pk_mul_f32 v[162:163], v[182:183], v[162:163]
	v_pk_mul_f32 v[160:161], v[180:181], v[160:161]
	v_pk_mul_f32 v[166:167], v[186:187], v[166:167]
	v_pk_mul_f32 v[164:165], v[184:185], v[164:165]
	v_pk_mul_f32 v[170:171], v[154:155], v[170:171]
	v_pk_mul_f32 v[168:169], v[188:189], v[168:169]
	v_cvt_pk_bf16_f32 v154, v156, v157
	v_cvt_pk_bf16_f32 v155, v158, v159
	v_cvt_pk_bf16_f32 v156, v160, v161
	v_cvt_pk_bf16_f32 v157, v162, v163
	v_cvt_pk_bf16_f32 v158, v164, v165
	v_cvt_pk_bf16_f32 v159, v166, v167
	v_cvt_pk_bf16_f32 v160, v168, v169
	v_cvt_pk_bf16_f32 v161, v170, v171
	global_store_dwordx4 v[148:149], v[154:157], off
	global_store_dwordx4 v[148:149], v[158:161], off offset:256
	v_cvt_f32_i32_e32 v157, v51
	v_cvt_f32_i32_e32 v156, v50
	v_cvt_f32_i32_e32 v159, v53
	v_cvt_f32_i32_e32 v158, v52
	v_cvt_f32_i32_e32 v161, v63
	v_cvt_f32_i32_e32 v160, v62
	v_cvt_f32_i32_e32 v163, v65
	v_cvt_f32_i32_e32 v162, v64
	v_cvt_f32_i32_e32 v165, v55
	v_cvt_f32_i32_e32 v164, v54
	v_cvt_f32_i32_e32 v167, v57
	v_cvt_f32_i32_e32 v166, v56
	v_cvt_f32_i32_e32 v169, v67
	v_cvt_f32_i32_e32 v168, v66
	v_cvt_f32_i32_e32 v171, v69
	v_cvt_f32_i32_e32 v170, v68
	v_or_b32_e32 v174, 32, v150
	v_ashrrev_i32_e32 v175, 31, v174
	v_lshl_add_u64 v[176:177], v[174:175], 2, s[38:39]
	v_or_b32_e32 v150, 48, v150
	v_ashrrev_i32_e32 v151, 31, v150
	v_mov_b32_e32 v154, v233
	v_pk_mul_f32 v[178:179], v[142:143], v[154:155] op_sel_hi:[1,0]
	v_pk_mul_f32 v[180:181], v[144:145], v[154:155] op_sel_hi:[1,0]
	v_pk_mul_f32 v[182:183], v[138:139], v[154:155] op_sel_hi:[1,0]
	v_pk_mul_f32 v[184:185], v[140:141], v[154:155] op_sel_hi:[1,0]
	v_pk_mul_f32 v[186:187], v[134:135], v[154:155] op_sel_hi:[1,0]
	v_pk_mul_f32 v[188:189], v[136:137], v[154:155] op_sel_hi:[1,0]
	v_pk_mul_f32 v[190:191], v[130:131], v[154:155] op_sel_hi:[1,0]
	v_pk_mul_f32 v[154:155], v[132:133], v[154:155] op_sel_hi:[1,0]
	v_pk_mul_f32 v[158:159], v[180:181], v[158:159]
	v_pk_mul_f32 v[156:157], v[178:179], v[156:157]
	v_pk_mul_f32 v[162:163], v[184:185], v[162:163]
	v_pk_mul_f32 v[160:161], v[182:183], v[160:161]
	v_pk_mul_f32 v[166:167], v[188:189], v[166:167]
	v_pk_mul_f32 v[164:165], v[186:187], v[164:165]
	v_pk_mul_f32 v[170:171], v[154:155], v[170:171]
	v_pk_mul_f32 v[168:169], v[190:191], v[168:169]
	v_cvt_pk_bf16_f32 v154, v156, v157
	v_cvt_pk_bf16_f32 v155, v158, v159
	v_cvt_pk_bf16_f32 v156, v160, v161
	v_cvt_pk_bf16_f32 v157, v162, v163
	v_cvt_pk_bf16_f32 v158, v164, v165
	v_cvt_pk_bf16_f32 v159, v166, v167
	v_cvt_pk_bf16_f32 v160, v168, v169
	v_cvt_pk_bf16_f32 v161, v170, v171
	global_store_dwordx4 v[172:173], v[154:157], off
	global_store_dwordx4 v[172:173], v[158:161], off offset:256
	v_cvt_f32_i32_e32 v157, v83
	v_cvt_f32_i32_e32 v156, v82
	v_cvt_f32_i32_e32 v159, v85
	v_cvt_f32_i32_e32 v158, v84
	v_cvt_f32_i32_e32 v161, v95
	v_cvt_f32_i32_e32 v160, v94
	v_cvt_f32_i32_e32 v163, v97
	v_cvt_f32_i32_e32 v162, v96
	v_cvt_f32_i32_e32 v165, v87
	v_cvt_f32_i32_e32 v164, v86
	v_cvt_f32_i32_e32 v167, v89
	v_cvt_f32_i32_e32 v166, v88
	v_cvt_f32_i32_e32 v169, v99
	v_cvt_f32_i32_e32 v168, v98
	v_cvt_f32_i32_e32 v171, v101
	v_cvt_f32_i32_e32 v170, v100
	v_lshlrev_b64 v[172:173], 12, v[174:175]
	v_lshl_add_u64 v[172:173], s[36:37], 0, v[172:173]
	v_lshl_add_u64 v[172:173], v[172:173], 0, v[152:153]
	v_lshl_add_u64 v[174:175], v[150:151], 2, s[38:39]
	v_lshlrev_b64 v[150:151], 12, v[150:151]
	v_lshl_add_u64 v[150:151], s[36:37], 0, v[150:151]
	v_mov_b32_e32 v154, v234
	v_pk_mul_f32 v[176:177], v[142:143], v[154:155] op_sel_hi:[1,0]
	v_pk_mul_f32 v[178:179], v[144:145], v[154:155] op_sel_hi:[1,0]
	v_pk_mul_f32 v[180:181], v[138:139], v[154:155] op_sel_hi:[1,0]
	v_pk_mul_f32 v[182:183], v[140:141], v[154:155] op_sel_hi:[1,0]
	v_pk_mul_f32 v[184:185], v[134:135], v[154:155] op_sel_hi:[1,0]
	v_pk_mul_f32 v[186:187], v[136:137], v[154:155] op_sel_hi:[1,0]
	v_pk_mul_f32 v[188:189], v[130:131], v[154:155] op_sel_hi:[1,0]
	v_pk_mul_f32 v[154:155], v[132:133], v[154:155] op_sel_hi:[1,0]
	v_pk_mul_f32 v[158:159], v[178:179], v[158:159]
	v_pk_mul_f32 v[156:157], v[176:177], v[156:157]
	v_pk_mul_f32 v[162:163], v[182:183], v[162:163]
	v_pk_mul_f32 v[160:161], v[180:181], v[160:161]
	v_pk_mul_f32 v[166:167], v[186:187], v[166:167]
	v_pk_mul_f32 v[164:165], v[184:185], v[164:165]
	v_pk_mul_f32 v[170:171], v[154:155], v[170:171]
	v_pk_mul_f32 v[168:169], v[188:189], v[168:169]
	v_cvt_pk_bf16_f32 v154, v156, v157
	v_cvt_pk_bf16_f32 v155, v158, v159
	v_cvt_pk_bf16_f32 v156, v160, v161
	v_cvt_pk_bf16_f32 v157, v162, v163
	v_cvt_pk_bf16_f32 v158, v164, v165
	v_cvt_pk_bf16_f32 v159, v166, v167
	v_cvt_pk_bf16_f32 v160, v168, v169
	v_cvt_pk_bf16_f32 v161, v170, v171
	global_store_dwordx4 v[172:173], v[154:157], off
	global_store_dwordx4 v[172:173], v[158:161], off offset:256
	v_cvt_f32_i32_e32 v157, v115
	v_cvt_f32_i32_e32 v156, v114
	v_cvt_f32_i32_e32 v159, v117
	v_cvt_f32_i32_e32 v158, v116
	v_cvt_f32_i32_e32 v161, v123
	v_cvt_f32_i32_e32 v160, v122
	v_cvt_f32_i32_e32 v163, v125
	v_cvt_f32_i32_e32 v162, v124
	v_cvt_f32_i32_e32 v165, v119
	v_cvt_f32_i32_e32 v164, v118
	v_cvt_f32_i32_e32 v167, v121
	v_cvt_f32_i32_e32 v166, v120
	v_cvt_f32_i32_e32 v169, v127
	v_cvt_f32_i32_e32 v168, v126
	v_cvt_f32_i32_e32 v171, v129
	v_cvt_f32_i32_e32 v170, v128
	v_lshl_add_u64 v[172:173], v[150:151], 0, v[152:153]
	v_mov_b32_e32 v154, v235
	v_pk_mul_f32 v[150:151], v[142:143], v[154:155] op_sel_hi:[1,0]
	v_pk_mul_f32 v[152:153], v[144:145], v[154:155] op_sel_hi:[1,0]
	v_pk_mul_f32 v[174:175], v[138:139], v[154:155] op_sel_hi:[1,0]
	v_pk_mul_f32 v[176:177], v[140:141], v[154:155] op_sel_hi:[1,0]
	v_pk_mul_f32 v[178:179], v[134:135], v[154:155] op_sel_hi:[1,0]
	v_pk_mul_f32 v[180:181], v[136:137], v[154:155] op_sel_hi:[1,0]
	v_pk_mul_f32 v[182:183], v[130:131], v[154:155] op_sel_hi:[1,0]
	v_pk_mul_f32 v[154:155], v[132:133], v[154:155] op_sel_hi:[1,0]
	v_pk_mul_f32 v[152:153], v[152:153], v[158:159]
	v_pk_mul_f32 v[150:151], v[150:151], v[156:157]
	v_pk_mul_f32 v[156:157], v[176:177], v[162:163]
	v_pk_mul_f32 v[158:159], v[174:175], v[160:161]
	v_pk_mul_f32 v[160:161], v[180:181], v[166:167]
	v_pk_mul_f32 v[162:163], v[178:179], v[164:165]
	v_pk_mul_f32 v[164:165], v[154:155], v[170:171]
	v_pk_mul_f32 v[166:167], v[182:183], v[168:169]
	v_cvt_pk_bf16_f32 v150, v150, v151
	v_cvt_pk_bf16_f32 v151, v152, v153
	v_cvt_pk_bf16_f32 v152, v158, v159
	v_cvt_pk_bf16_f32 v153, v156, v157
	v_cvt_pk_bf16_f32 v154, v162, v163
	v_cvt_pk_bf16_f32 v155, v160, v161
	v_cvt_pk_bf16_f32 v156, v166, v167
	v_cvt_pk_bf16_f32 v157, v164, v165
	global_store_dwordx4 v[172:173], v[150:153], off
	global_store_dwordx4 v[172:173], v[154:157], off offset:256
	v_cvt_f32_i32_e32 v153, v3
	v_cvt_f32_i32_e32 v152, v2
	v_cvt_f32_i32_e32 v155, v5
	v_cvt_f32_i32_e32 v154, v4
	v_cvt_f32_i32_e32 v157, v7
	v_cvt_f32_i32_e32 v156, v6
	v_cvt_f32_i32_e32 v159, v9
	v_cvt_f32_i32_e32 v158, v8
	v_cvt_f32_i32_e32 v161, v11
	v_cvt_f32_i32_e32 v160, v10
	v_cvt_f32_i32_e32 v163, v13
	v_cvt_f32_i32_e32 v162, v12
	v_cvt_f32_i32_e32 v165, v15
	v_cvt_f32_i32_e32 v164, v14
	v_cvt_f32_i32_e32 v167, v17
	v_cvt_f32_i32_e32 v166, v16
	v_add_co_u32_e32 v170, vcc, s28, v148
	v_lshl_add_u64 v[168:169], v[148:149], 0, s[2:3]
	s_nop 0
	v_addc_co_u32_e32 v171, vcc, 0, v149, vcc
	s_mov_b32 s28, 0x90000
	s_mov_b64 s[2:3], 0x90000
	v_mov_b32_e32 v150, v236
	v_pk_mul_f32 v[172:173], v[142:143], v[150:151] op_sel_hi:[1,0]
	v_pk_mul_f32 v[174:175], v[144:145], v[150:151] op_sel_hi:[1,0]
	v_pk_mul_f32 v[176:177], v[138:139], v[150:151] op_sel_hi:[1,0]
	v_pk_mul_f32 v[178:179], v[140:141], v[150:151] op_sel_hi:[1,0]
	v_pk_mul_f32 v[180:181], v[134:135], v[150:151] op_sel_hi:[1,0]
	v_pk_mul_f32 v[182:183], v[136:137], v[150:151] op_sel_hi:[1,0]
	v_pk_mul_f32 v[184:185], v[130:131], v[150:151] op_sel_hi:[1,0]
	v_pk_mul_f32 v[150:151], v[132:133], v[150:151] op_sel_hi:[1,0]
	v_pk_mul_f32 v[154:155], v[174:175], v[154:155]
	v_pk_mul_f32 v[152:153], v[172:173], v[152:153]
	v_pk_mul_f32 v[158:159], v[178:179], v[158:159]
	v_pk_mul_f32 v[156:157], v[176:177], v[156:157]
	v_pk_mul_f32 v[162:163], v[182:183], v[162:163]
	v_pk_mul_f32 v[160:161], v[180:181], v[160:161]
	v_pk_mul_f32 v[166:167], v[150:151], v[166:167]
	v_pk_mul_f32 v[164:165], v[184:185], v[164:165]
	v_cvt_pk_bf16_f32 v150, v152, v153
	v_cvt_pk_bf16_f32 v151, v154, v155
	v_cvt_pk_bf16_f32 v152, v156, v157
	v_cvt_pk_bf16_f32 v153, v158, v159
	v_cvt_pk_bf16_f32 v154, v160, v161
	v_cvt_pk_bf16_f32 v155, v162, v163
	v_cvt_pk_bf16_f32 v156, v164, v165
	v_cvt_pk_bf16_f32 v157, v166, v167
	global_store_dwordx4 v[170:171], v[150:153], off
	global_store_dwordx4 v[168:169], v[154:157], off offset:256
	v_cvt_f32_i32_e32 v153, v31
	v_cvt_f32_i32_e32 v152, v30
	v_cvt_f32_i32_e32 v155, v33
	v_cvt_f32_i32_e32 v154, v32
	v_cvt_f32_i32_e32 v157, v43
	v_cvt_f32_i32_e32 v156, v42
	v_cvt_f32_i32_e32 v159, v45
	v_cvt_f32_i32_e32 v158, v44
	v_cvt_f32_i32_e32 v161, v39
	v_cvt_f32_i32_e32 v160, v38
	v_cvt_f32_i32_e32 v163, v41
	v_cvt_f32_i32_e32 v162, v40
	v_cvt_f32_i32_e32 v165, v47
	v_cvt_f32_i32_e32 v164, v46
	v_cvt_f32_i32_e32 v167, v49
	v_cvt_f32_i32_e32 v166, v48
	v_add_co_u32_e32 v170, vcc, s28, v148
	v_lshl_add_u64 v[168:169], v[148:149], 0, s[2:3]
	s_nop 0
	v_addc_co_u32_e32 v171, vcc, 0, v149, vcc
	s_mov_b32 s28, 0xa0000
	s_mov_b64 s[2:3], 0xa0000
	v_mov_b32_e32 v150, v237
	v_pk_mul_f32 v[172:173], v[142:143], v[150:151] op_sel_hi:[1,0]
	v_pk_mul_f32 v[174:175], v[144:145], v[150:151] op_sel_hi:[1,0]
	v_pk_mul_f32 v[176:177], v[138:139], v[150:151] op_sel_hi:[1,0]
	v_pk_mul_f32 v[178:179], v[140:141], v[150:151] op_sel_hi:[1,0]
	v_pk_mul_f32 v[180:181], v[134:135], v[150:151] op_sel_hi:[1,0]
	v_pk_mul_f32 v[182:183], v[136:137], v[150:151] op_sel_hi:[1,0]
	v_pk_mul_f32 v[184:185], v[130:131], v[150:151] op_sel_hi:[1,0]
	v_pk_mul_f32 v[150:151], v[132:133], v[150:151] op_sel_hi:[1,0]
	v_pk_mul_f32 v[154:155], v[174:175], v[154:155]
	v_pk_mul_f32 v[152:153], v[172:173], v[152:153]
	v_pk_mul_f32 v[158:159], v[178:179], v[158:159]
	v_pk_mul_f32 v[156:157], v[176:177], v[156:157]
	v_pk_mul_f32 v[162:163], v[182:183], v[162:163]
	v_pk_mul_f32 v[160:161], v[180:181], v[160:161]
	v_pk_mul_f32 v[166:167], v[150:151], v[166:167]
	v_pk_mul_f32 v[164:165], v[184:185], v[164:165]
	v_cvt_pk_bf16_f32 v150, v152, v153
	v_cvt_pk_bf16_f32 v151, v154, v155
	v_cvt_pk_bf16_f32 v152, v156, v157
	v_cvt_pk_bf16_f32 v153, v158, v159
	v_cvt_pk_bf16_f32 v154, v160, v161
	v_cvt_pk_bf16_f32 v155, v162, v163
	v_cvt_pk_bf16_f32 v156, v164, v165
	v_cvt_pk_bf16_f32 v157, v166, v167
	global_store_dwordx4 v[170:171], v[150:153], off
	global_store_dwordx4 v[168:169], v[154:157], off offset:256
	v_cvt_f32_i32_e32 v153, v59
	v_cvt_f32_i32_e32 v152, v58
	v_cvt_f32_i32_e32 v155, v61
	v_cvt_f32_i32_e32 v154, v60
	v_cvt_f32_i32_e32 v157, v75
	v_cvt_f32_i32_e32 v156, v74
	v_cvt_f32_i32_e32 v159, v77
	v_cvt_f32_i32_e32 v158, v76
	v_cvt_f32_i32_e32 v161, v71
	v_cvt_f32_i32_e32 v160, v70
	v_cvt_f32_i32_e32 v163, v73
	v_cvt_f32_i32_e32 v162, v72
	v_cvt_f32_i32_e32 v165, v79
	v_cvt_f32_i32_e32 v164, v78
	v_cvt_f32_i32_e32 v167, v81
	v_cvt_f32_i32_e32 v166, v80
	v_add_co_u32_e32 v170, vcc, s28, v148
	v_lshl_add_u64 v[168:169], v[148:149], 0, s[2:3]
	s_nop 0
	v_addc_co_u32_e32 v171, vcc, 0, v149, vcc
	s_andn2_b64 vcc, exec, s[0:1]
	v_mov_b32_e32 v150, v238
	v_pk_mul_f32 v[172:173], v[142:143], v[150:151] op_sel_hi:[1,0]
	v_pk_mul_f32 v[174:175], v[144:145], v[150:151] op_sel_hi:[1,0]
	v_pk_mul_f32 v[176:177], v[138:139], v[150:151] op_sel_hi:[1,0]
	v_pk_mul_f32 v[178:179], v[140:141], v[150:151] op_sel_hi:[1,0]
	v_pk_mul_f32 v[180:181], v[134:135], v[150:151] op_sel_hi:[1,0]
	v_pk_mul_f32 v[182:183], v[136:137], v[150:151] op_sel_hi:[1,0]
	v_pk_mul_f32 v[184:185], v[130:131], v[150:151] op_sel_hi:[1,0]
	v_pk_mul_f32 v[150:151], v[132:133], v[150:151] op_sel_hi:[1,0]
	v_pk_mul_f32 v[154:155], v[174:175], v[154:155]
	v_pk_mul_f32 v[152:153], v[172:173], v[152:153]
	v_pk_mul_f32 v[158:159], v[178:179], v[158:159]
	v_pk_mul_f32 v[156:157], v[176:177], v[156:157]
	v_pk_mul_f32 v[162:163], v[182:183], v[162:163]
	v_pk_mul_f32 v[160:161], v[180:181], v[160:161]
	v_pk_mul_f32 v[166:167], v[150:151], v[166:167]
	v_pk_mul_f32 v[164:165], v[184:185], v[164:165]
	v_cvt_pk_bf16_f32 v150, v152, v153
	v_cvt_pk_bf16_f32 v151, v154, v155
	v_cvt_pk_bf16_f32 v152, v156, v157
	v_cvt_pk_bf16_f32 v153, v158, v159
	v_cvt_pk_bf16_f32 v154, v160, v161
	v_cvt_pk_bf16_f32 v155, v162, v163
	v_cvt_pk_bf16_f32 v156, v164, v165
	v_cvt_pk_bf16_f32 v157, v166, v167
	global_store_dwordx4 v[170:171], v[150:153], off
	global_store_dwordx4 v[168:169], v[154:157], off offset:256
	v_cvt_f32_i32_e32 v151, v91
	v_cvt_f32_i32_e32 v150, v90
	v_cvt_f32_i32_e32 v153, v93
	v_cvt_f32_i32_e32 v152, v92
	v_cvt_f32_i32_e32 v155, v107
	v_cvt_f32_i32_e32 v154, v106
	v_cvt_f32_i32_e32 v157, v109
	v_cvt_f32_i32_e32 v156, v108
	v_cvt_f32_i32_e32 v159, v103
	v_cvt_f32_i32_e32 v158, v102
	v_cvt_f32_i32_e32 v161, v105
	v_cvt_f32_i32_e32 v160, v104
	v_cvt_f32_i32_e32 v163, v111
	v_cvt_f32_i32_e32 v162, v110
	v_cvt_f32_i32_e32 v165, v113
	v_cvt_f32_i32_e32 v164, v112
	v_lshl_add_u64 v[166:167], v[148:149], 0, s[18:19]
	v_add_co_u32_e64 v148, s[0:1], s73, v148
	v_mov_b32_e32 v146, v239
	v_pk_mul_f32 v[142:143], v[142:143], v[146:147] op_sel_hi:[1,0]
	v_pk_mul_f32 v[144:145], v[144:145], v[146:147] op_sel_hi:[1,0]
	v_pk_mul_f32 v[138:139], v[138:139], v[146:147] op_sel_hi:[1,0]
	v_pk_mul_f32 v[140:141], v[140:141], v[146:147] op_sel_hi:[1,0]
	v_addc_co_u32_e64 v149, s[0:1], 0, v149, s[0:1]
	v_pk_mul_f32 v[134:135], v[134:135], v[146:147] op_sel_hi:[1,0]
	v_pk_mul_f32 v[136:137], v[136:137], v[146:147] op_sel_hi:[1,0]
	v_pk_mul_f32 v[130:131], v[130:131], v[146:147] op_sel_hi:[1,0]
	v_pk_mul_f32 v[132:133], v[132:133], v[146:147] op_sel_hi:[1,0]
	v_pk_mul_f32 v[144:145], v[144:145], v[152:153]
	v_pk_mul_f32 v[142:143], v[142:143], v[150:151]
	v_pk_mul_f32 v[140:141], v[140:141], v[156:157]
	v_pk_mul_f32 v[138:139], v[138:139], v[154:155]
	v_pk_mul_f32 v[136:137], v[136:137], v[160:161]
	v_pk_mul_f32 v[134:135], v[134:135], v[158:159]
	v_pk_mul_f32 v[146:147], v[132:133], v[164:165]
	v_pk_mul_f32 v[150:151], v[130:131], v[162:163]
	v_cvt_pk_bf16_f32 v130, v142, v143
	v_cvt_pk_bf16_f32 v131, v144, v145
	v_cvt_pk_bf16_f32 v132, v138, v139
	v_cvt_pk_bf16_f32 v133, v140, v141
	s_mov_b64 s[0:1], -1
	v_cvt_pk_bf16_f32 v134, v134, v135
	v_cvt_pk_bf16_f32 v135, v136, v137
	v_cvt_pk_bf16_f32 v136, v150, v151
	v_cvt_pk_bf16_f32 v137, v146, v147
	global_store_dwordx4 v[148:149], v[130:133], off
	global_store_dwordx4 v[166:167], v[134:137], off offset:256
	s_cbranch_vccnz .LBB0_1082
	s_andn2_b64 vcc, exec, s[6:7]
	s_cbranch_vccnz .LBB0_1081
	s_barrier
	s_branch .LBB0_1081
